# v29 with the bf16 8-read load segments back to full pre-barrier LDS waits (late fragment reads only in the 16-read bf16 segments)
# speedup vs baseline: 1.0041x; 1.0041x over previous
.LBB0_219:
	s_waitcnt lgkmcnt(0)
	s_add_i32 s4, s92, 0x180
	s_add_i32 s5, s93, 0x180
	s_barrier
	s_setprio 1
	s_waitcnt lgkmcnt(7)
	v_mfma_f32_16x16x32_bf16 v[60:63], v[156:159], v[188:191], 0
	s_waitcnt lgkmcnt(6)
	v_mfma_f32_16x16x32_bf16 v[60:63], v[152:155], v[184:187], v[60:63]
	v_mfma_f32_16x16x32_bf16 v[56:59], v[148:151], v[188:191], 0
	s_nop 0
	v_mfma_f32_16x16x32_bf16 v[56:59], v[144:147], v[184:187], v[56:59]
	s_waitcnt lgkmcnt(5)
	v_mfma_f32_16x16x32_bf16 v[52:55], v[156:159], v[180:183], 0
	s_waitcnt lgkmcnt(4)
	v_mfma_f32_16x16x32_bf16 v[52:55], v[152:155], v[176:179], v[52:55]
	v_mfma_f32_16x16x32_bf16 v[48:51], v[148:151], v[180:183], 0
	s_nop 0
	v_mfma_f32_16x16x32_bf16 v[48:51], v[144:147], v[176:179], v[48:51]
	s_waitcnt lgkmcnt(3)
	v_mfma_f32_16x16x32_bf16 v[44:47], v[156:159], v[172:175], 0
	s_waitcnt lgkmcnt(2)
	v_mfma_f32_16x16x32_bf16 v[44:47], v[152:155], v[168:171], v[44:47]
	v_mfma_f32_16x16x32_bf16 v[40:43], v[148:151], v[172:175], 0
	s_nop 0
	v_mfma_f32_16x16x32_bf16 v[40:43], v[144:147], v[168:171], v[40:43]
	s_waitcnt lgkmcnt(1)
	v_mfma_f32_16x16x32_bf16 v[36:39], v[156:159], v[164:167], 0
	s_waitcnt lgkmcnt(0)
	v_mfma_f32_16x16x32_bf16 v[36:39], v[152:155], v[160:163], v[36:39]
	v_mfma_f32_16x16x32_bf16 v[32:35], v[148:151], v[164:167], 0
	s_nop 0
	v_mfma_f32_16x16x32_bf16 v[32:35], v[144:147], v[160:163], v[32:35]
	s_setprio 0
	s_setprio 1
	v_mfma_f32_16x16x32_bf16 v[28:31], v[140:143], v[188:191], 0
	s_nop 0
	v_mfma_f32_16x16x32_bf16 v[28:31], v[136:139], v[184:187], v[28:31]
	v_mfma_f32_16x16x32_bf16 v[24:27], v[132:135], v[188:191], 0
	s_nop 0
	v_mfma_f32_16x16x32_bf16 v[24:27], v[128:131], v[184:187], v[24:27]
	v_mfma_f32_16x16x32_bf16 v[20:23], v[140:143], v[180:183], 0
	s_nop 0
	v_mfma_f32_16x16x32_bf16 v[20:23], v[136:139], v[176:179], v[20:23]
	v_mfma_f32_16x16x32_bf16 v[16:19], v[132:135], v[180:183], 0
	s_nop 0
	v_mfma_f32_16x16x32_bf16 v[16:19], v[128:131], v[176:179], v[16:19]
	v_mfma_f32_16x16x32_bf16 v[12:15], v[140:143], v[172:175], 0
	s_nop 0
	v_mfma_f32_16x16x32_bf16 v[12:15], v[136:139], v[168:171], v[12:15]
	v_mfma_f32_16x16x32_bf16 v[8:11], v[132:135], v[172:175], 0
	s_nop 0
	v_mfma_f32_16x16x32_bf16 v[8:11], v[128:131], v[168:171], v[8:11]
	v_mfma_f32_16x16x32_bf16 v[4:7], v[140:143], v[164:167], 0
	s_nop 0
	v_mfma_f32_16x16x32_bf16 v[4:7], v[136:139], v[160:163], v[4:7]
	v_mfma_f32_16x16x32_bf16 v[0:3], v[132:135], v[164:167], 0
	s_nop 0
	v_mfma_f32_16x16x32_bf16 v[0:3], v[128:131], v[160:163], v[0:3]
	s_setprio 0
	s_barrier
	ds_read_b128 v[156:159], v211
	ds_read_b128 v[152:155], v212
	ds_read_b128 v[148:151], v213
	ds_read_b128 v[144:147], v214
	ds_read_b128 v[140:143], v215
	ds_read_b128 v[136:139], v216
	ds_read_b128 v[132:135], v217
	ds_read_b128 v[128:131], v218
	ds_read_b128 v[160:163], v219 offset:32768
	ds_read_b128 v[164:167], v219 offset:33792
	ds_read_b128 v[168:171], v219 offset:34816
	ds_read_b128 v[172:175], v219 offset:35840
	ds_read_b128 v[176:179], v219 offset:36864
	ds_read_b128 v[180:183], v219 offset:37888
	ds_read_b128 v[184:187], v219 offset:38912
	ds_read_b128 v[188:191], v219 offset:39936
	s_mov_b32 m0, s69
	s_add_i32 s14, s92, 0x20100
	buffer_load_dwordx4 v196, s[8:11], s14 offen lds
	s_add_i32 s14, s92, 0x30100
	s_mov_b32 m0, s70
	s_nop 0
	buffer_load_dwordx4 v196, s[8:11], s14 offen lds
	s_waitcnt vmcnt(8)
	s_waitcnt lgkmcnt(8)
	s_barrier
	s_setprio 1
	s_waitcnt lgkmcnt(7)
	v_mfma_f32_16x16x32_bf16 v[124:127], v[156:159], v[160:163], v[124:127]
	s_waitcnt lgkmcnt(6)
	v_mfma_f32_16x16x32_bf16 v[124:127], v[152:155], v[164:167], v[124:127]
	v_mfma_f32_16x16x32_bf16 v[120:123], v[148:151], v[160:163], v[120:123]
	s_nop 0
	v_mfma_f32_16x16x32_bf16 v[120:123], v[144:147], v[164:167], v[120:123]
	s_waitcnt lgkmcnt(5)
	v_mfma_f32_16x16x32_bf16 v[116:119], v[156:159], v[168:171], v[116:119]
	s_waitcnt lgkmcnt(4)
	v_mfma_f32_16x16x32_bf16 v[116:119], v[152:155], v[172:175], v[116:119]
	v_mfma_f32_16x16x32_bf16 v[112:115], v[148:151], v[168:171], v[112:115]
	s_nop 0
	v_mfma_f32_16x16x32_bf16 v[112:115], v[144:147], v[172:175], v[112:115]
	s_waitcnt lgkmcnt(3)
	v_mfma_f32_16x16x32_bf16 v[108:111], v[156:159], v[176:179], v[108:111]
	s_waitcnt lgkmcnt(2)
	v_mfma_f32_16x16x32_bf16 v[108:111], v[152:155], v[180:183], v[108:111]
	v_mfma_f32_16x16x32_bf16 v[104:107], v[148:151], v[176:179], v[104:107]
	s_nop 0
	v_mfma_f32_16x16x32_bf16 v[104:107], v[144:147], v[180:183], v[104:107]
	s_waitcnt lgkmcnt(1)
	v_mfma_f32_16x16x32_bf16 v[100:103], v[156:159], v[184:187], v[100:103]
	s_waitcnt lgkmcnt(0)
	v_mfma_f32_16x16x32_bf16 v[100:103], v[152:155], v[188:191], v[100:103]
	v_mfma_f32_16x16x32_bf16 v[96:99], v[148:151], v[184:187], v[96:99]
	s_nop 0
	v_mfma_f32_16x16x32_bf16 v[96:99], v[144:147], v[188:191], v[96:99]
	s_setprio 0
	s_setprio 1
	v_mfma_f32_16x16x32_bf16 v[92:95], v[140:143], v[160:163], v[92:95]
	s_nop 0
	v_mfma_f32_16x16x32_bf16 v[92:95], v[136:139], v[164:167], v[92:95]
	v_mfma_f32_16x16x32_bf16 v[88:91], v[132:135], v[160:163], v[88:91]
	s_nop 0
	v_mfma_f32_16x16x32_bf16 v[88:91], v[128:131], v[164:167], v[88:91]
	v_mfma_f32_16x16x32_bf16 v[84:87], v[140:143], v[168:171], v[84:87]
	s_nop 0
	v_mfma_f32_16x16x32_bf16 v[84:87], v[136:139], v[172:175], v[84:87]
	v_mfma_f32_16x16x32_bf16 v[80:83], v[132:135], v[168:171], v[80:83]
	s_nop 0
	v_mfma_f32_16x16x32_bf16 v[80:83], v[128:131], v[172:175], v[80:83]
	v_mfma_f32_16x16x32_bf16 v[76:79], v[140:143], v[176:179], v[76:79]
	s_nop 0
	v_mfma_f32_16x16x32_bf16 v[76:79], v[136:139], v[180:183], v[76:79]
	v_mfma_f32_16x16x32_bf16 v[72:75], v[132:135], v[176:179], v[72:75]
	s_nop 0
	v_mfma_f32_16x16x32_bf16 v[72:75], v[128:131], v[180:183], v[72:75]
	v_mfma_f32_16x16x32_bf16 v[68:71], v[140:143], v[184:187], v[68:71]
	s_nop 0
	v_mfma_f32_16x16x32_bf16 v[68:71], v[136:139], v[188:191], v[68:71]
	v_mfma_f32_16x16x32_bf16 v[64:67], v[132:135], v[184:187], v[64:67]
	s_nop 0
	v_mfma_f32_16x16x32_bf16 v[64:67], v[128:131], v[188:191], v[64:67]
	s_setprio 0
	s_barrier
	ds_read_b128 v[160:163], v219 offset:49152
	ds_read_b128 v[164:167], v219 offset:50176
	ds_read_b128 v[168:171], v219 offset:51200
	ds_read_b128 v[172:175], v219 offset:52224
	ds_read_b128 v[176:179], v219 offset:53248
	ds_read_b128 v[180:183], v219 offset:54272
	ds_read_b128 v[184:187], v219 offset:55296
	ds_read_b128 v[188:191], v219 offset:56320
	s_mov_b32 m0, s73
	s_mov_b32 s14, s10
	s_mov_b32 s15, s11
	buffer_load_dwordx4 v202, s[12:15], s5 offen lds
	s_add_i32 s5, s93, 0x80180
	s_mov_b32 m0, s74
	s_nop 0
	buffer_load_dwordx4 v202, s[12:15], s5 offen lds
	s_add_i32 s5, s93, 0x8180
	s_mov_b32 m0, s77
	s_nop 0
	buffer_load_dwordx4 v202, s[12:15], s5 offen lds
	s_add_i32 s5, s93, 0x88180
	s_mov_b32 m0, s78
	s_nop 0
	buffer_load_dwordx4 v202, s[12:15], s5 offen lds
	s_mov_b32 m0, s75
	s_nop 0
	buffer_load_dwordx4 v196, s[8:11], s4 offen lds
	s_add_i32 s4, s92, 0x10180
	s_mov_b32 m0, s76
	s_nop 0
	buffer_load_dwordx4 v196, s[8:11], s4 offen lds
	s_waitcnt vmcnt(8)
	s_waitcnt lgkmcnt(0)
	s_barrier
	s_setprio 1
	s_waitcnt lgkmcnt(7)
	v_mfma_f32_16x16x32_bf16 v[60:63], v[156:159], v[160:163], v[60:63]
	s_waitcnt lgkmcnt(6)
	v_mfma_f32_16x16x32_bf16 v[60:63], v[152:155], v[164:167], v[60:63]
	v_mfma_f32_16x16x32_bf16 v[56:59], v[148:151], v[160:163], v[56:59]
	s_nop 0
	v_mfma_f32_16x16x32_bf16 v[56:59], v[144:147], v[164:167], v[56:59]
	s_waitcnt lgkmcnt(5)
	v_mfma_f32_16x16x32_bf16 v[52:55], v[156:159], v[168:171], v[52:55]
	s_waitcnt lgkmcnt(4)
	v_mfma_f32_16x16x32_bf16 v[52:55], v[152:155], v[172:175], v[52:55]
	v_mfma_f32_16x16x32_bf16 v[48:51], v[148:151], v[168:171], v[48:51]
	s_nop 0
	v_mfma_f32_16x16x32_bf16 v[48:51], v[144:147], v[172:175], v[48:51]
	s_waitcnt lgkmcnt(3)
	v_mfma_f32_16x16x32_bf16 v[44:47], v[156:159], v[176:179], v[44:47]
	s_waitcnt lgkmcnt(2)
	v_mfma_f32_16x16x32_bf16 v[44:47], v[152:155], v[180:183], v[44:47]
	v_mfma_f32_16x16x32_bf16 v[40:43], v[148:151], v[176:179], v[40:43]
	s_nop 0
	v_mfma_f32_16x16x32_bf16 v[40:43], v[144:147], v[180:183], v[40:43]
	s_waitcnt lgkmcnt(1)
	v_mfma_f32_16x16x32_bf16 v[36:39], v[156:159], v[184:187], v[36:39]
	s_waitcnt lgkmcnt(0)
	v_mfma_f32_16x16x32_bf16 v[36:39], v[152:155], v[188:191], v[36:39]
	v_mfma_f32_16x16x32_bf16 v[32:35], v[148:151], v[184:187], v[32:35]
	s_nop 0
	v_mfma_f32_16x16x32_bf16 v[32:35], v[144:147], v[188:191], v[32:35]
	s_setprio 0
	s_setprio 1
	v_mfma_f32_16x16x32_bf16 v[28:31], v[140:143], v[160:163], v[28:31]
	s_nop 0
	v_mfma_f32_16x16x32_bf16 v[28:31], v[136:139], v[164:167], v[28:31]
	v_mfma_f32_16x16x32_bf16 v[24:27], v[132:135], v[160:163], v[24:27]
	s_nop 0
	v_mfma_f32_16x16x32_bf16 v[24:27], v[128:131], v[164:167], v[24:27]
	v_mfma_f32_16x16x32_bf16 v[20:23], v[140:143], v[168:171], v[20:23]
	s_nop 0
	v_mfma_f32_16x16x32_bf16 v[20:23], v[136:139], v[172:175], v[20:23]
	v_mfma_f32_16x16x32_bf16 v[16:19], v[132:135], v[168:171], v[16:19]
	s_nop 0
	v_mfma_f32_16x16x32_bf16 v[16:19], v[128:131], v[172:175], v[16:19]
	v_mfma_f32_16x16x32_bf16 v[12:15], v[140:143], v[176:179], v[12:15]
	s_nop 0
	v_mfma_f32_16x16x32_bf16 v[12:15], v[136:139], v[180:183], v[12:15]
	v_mfma_f32_16x16x32_bf16 v[8:11], v[132:135], v[176:179], v[8:11]
	s_nop 0
	v_mfma_f32_16x16x32_bf16 v[8:11], v[128:131], v[180:183], v[8:11]
	v_mfma_f32_16x16x32_bf16 v[4:7], v[140:143], v[184:187], v[4:7]
	s_nop 0
	v_mfma_f32_16x16x32_bf16 v[4:7], v[136:139], v[188:191], v[4:7]
	v_mfma_f32_16x16x32_bf16 v[0:3], v[132:135], v[184:187], v[0:3]
	s_nop 0
	v_mfma_f32_16x16x32_bf16 v[0:3], v[128:131], v[188:191], v[0:3]
	s_setprio 0
	s_barrier
	s_add_i32 s4, s92, 0x30180
	s_add_i32 s5, s93, 0x200
	s_mov_b32 s33, 0
.LBB0_220:
	ds_read_b128 v[128:131], v203
	ds_read_b128 v[132:135], v204
	ds_read_b128 v[136:139], v205
	ds_read_b128 v[140:143], v206
	ds_read_b128 v[144:147], v207
	ds_read_b128 v[148:151], v208
	ds_read_b128 v[152:155], v209
	ds_read_b128 v[156:159], v210
	ds_read_b128 v[160:163], v219
	ds_read_b128 v[164:167], v219 offset:1024
	ds_read_b128 v[168:171], v219 offset:2048
	ds_read_b128 v[172:175], v219 offset:3072
	ds_read_b128 v[176:179], v219 offset:4096
	ds_read_b128 v[180:183], v219 offset:5120
	ds_read_b128 v[184:187], v219 offset:6144
	ds_read_b128 v[188:191], v219 offset:7168
	s_add_i32 s66, s4, 0xfffd0080
	s_cmp_eq_u32 s33, 4
	s_cselect_b32 s66, s90, s66
	s_cselect_b32 s92, s91, s5
	s_add_i32 s67, s66, 0x80
	s_mov_b32 m0, s79
	s_add_i32 s93, s4, 0xffff0000
	buffer_load_dwordx4 v196, s[8:11], s93 offen lds
	s_mov_b32 m0, s81
	s_nop 0
	buffer_load_dwordx4 v196, s[8:11], s4 offen lds
	s_waitcnt vmcnt(8)
	s_waitcnt lgkmcnt(8)
	s_barrier
	s_setprio 1
	s_waitcnt lgkmcnt(7)
	v_mfma_f32_16x16x32_bf16 v[124:127], v[128:131], v[160:163], v[124:127]
	s_waitcnt lgkmcnt(6)
	v_mfma_f32_16x16x32_bf16 v[124:127], v[132:135], v[164:167], v[124:127]
	v_mfma_f32_16x16x32_bf16 v[120:123], v[136:139], v[160:163], v[120:123]
	s_nop 0
	v_mfma_f32_16x16x32_bf16 v[120:123], v[140:143], v[164:167], v[120:123]
	s_waitcnt lgkmcnt(5)
	v_mfma_f32_16x16x32_bf16 v[116:119], v[128:131], v[168:171], v[116:119]
	s_waitcnt lgkmcnt(4)
	v_mfma_f32_16x16x32_bf16 v[116:119], v[132:135], v[172:175], v[116:119]
	v_mfma_f32_16x16x32_bf16 v[112:115], v[136:139], v[168:171], v[112:115]
	s_nop 0
	v_mfma_f32_16x16x32_bf16 v[112:115], v[140:143], v[172:175], v[112:115]
	s_waitcnt lgkmcnt(3)
	v_mfma_f32_16x16x32_bf16 v[108:111], v[128:131], v[176:179], v[108:111]
	s_waitcnt lgkmcnt(2)
	v_mfma_f32_16x16x32_bf16 v[108:111], v[132:135], v[180:183], v[108:111]
	v_mfma_f32_16x16x32_bf16 v[104:107], v[136:139], v[176:179], v[104:107]
	s_nop 0
	v_mfma_f32_16x16x32_bf16 v[104:107], v[140:143], v[180:183], v[104:107]
	s_waitcnt lgkmcnt(1)
	v_mfma_f32_16x16x32_bf16 v[100:103], v[128:131], v[184:187], v[100:103]
	s_waitcnt lgkmcnt(0)
	v_mfma_f32_16x16x32_bf16 v[100:103], v[132:135], v[188:191], v[100:103]
	v_mfma_f32_16x16x32_bf16 v[96:99], v[136:139], v[184:187], v[96:99]
	s_nop 0
	v_mfma_f32_16x16x32_bf16 v[96:99], v[140:143], v[188:191], v[96:99]
	s_setprio 0
	s_setprio 1
	v_mfma_f32_16x16x32_bf16 v[92:95], v[144:147], v[160:163], v[92:95]
	s_nop 0
	v_mfma_f32_16x16x32_bf16 v[92:95], v[148:151], v[164:167], v[92:95]
	v_mfma_f32_16x16x32_bf16 v[88:91], v[152:155], v[160:163], v[88:91]
	s_nop 0
	v_mfma_f32_16x16x32_bf16 v[88:91], v[156:159], v[164:167], v[88:91]
	v_mfma_f32_16x16x32_bf16 v[84:87], v[144:147], v[168:171], v[84:87]
	s_nop 0
	v_mfma_f32_16x16x32_bf16 v[84:87], v[148:151], v[172:175], v[84:87]
	v_mfma_f32_16x16x32_bf16 v[80:83], v[152:155], v[168:171], v[80:83]
	s_nop 0
	v_mfma_f32_16x16x32_bf16 v[80:83], v[156:159], v[172:175], v[80:83]
	v_mfma_f32_16x16x32_bf16 v[76:79], v[144:147], v[176:179], v[76:79]
	s_nop 0
	v_mfma_f32_16x16x32_bf16 v[76:79], v[148:151], v[180:183], v[76:79]
	v_mfma_f32_16x16x32_bf16 v[72:75], v[152:155], v[176:179], v[72:75]
	s_nop 0
	v_mfma_f32_16x16x32_bf16 v[72:75], v[156:159], v[180:183], v[72:75]
	v_mfma_f32_16x16x32_bf16 v[68:71], v[144:147], v[184:187], v[68:71]
	s_nop 0
	v_mfma_f32_16x16x32_bf16 v[68:71], v[148:151], v[188:191], v[68:71]
	v_mfma_f32_16x16x32_bf16 v[64:67], v[152:155], v[184:187], v[64:67]
	s_nop 0
	v_mfma_f32_16x16x32_bf16 v[64:67], v[156:159], v[188:191], v[64:67]
	s_setprio 0
	s_barrier
	ds_read_b128 v[160:163], v219 offset:16384
	ds_read_b128 v[164:167], v219 offset:17408
	ds_read_b128 v[168:171], v219 offset:18432
	ds_read_b128 v[172:175], v219 offset:19456
	ds_read_b128 v[176:179], v219 offset:20480
	ds_read_b128 v[180:183], v219 offset:21504
	ds_read_b128 v[184:187], v219 offset:22528
	ds_read_b128 v[188:191], v219 offset:23552
	s_mov_b32 m0, s62
	s_add_i32 s93, s92, 0x80000
	buffer_load_dwordx4 v202, s[12:15], s92 offen lds
	s_mov_b32 m0, s63
	s_nop 0
	buffer_load_dwordx4 v202, s[12:15], s93 offen lds
	s_add_i32 s93, s92, 0x8000
	s_mov_b32 m0, s64
	s_nop 0
	buffer_load_dwordx4 v202, s[12:15], s93 offen lds
	s_add_i32 s93, s92, 0x88000
	s_mov_b32 m0, s65
	s_nop 0
	buffer_load_dwordx4 v202, s[12:15], s93 offen lds
	s_mov_b32 m0, s45
	s_add_i32 s93, s66, 0x10000
	buffer_load_dwordx4 v196, s[8:11], s66 offen lds
	s_mov_b32 m0, s68
	s_nop 0
	buffer_load_dwordx4 v196, s[8:11], s93 offen lds
	s_waitcnt vmcnt(8)
	s_waitcnt lgkmcnt(0)
	s_barrier
	s_setprio 1
	s_waitcnt lgkmcnt(7)
	v_mfma_f32_16x16x32_bf16 v[60:63], v[128:131], v[160:163], v[60:63]
	s_waitcnt lgkmcnt(6)
	v_mfma_f32_16x16x32_bf16 v[60:63], v[132:135], v[164:167], v[60:63]
	v_mfma_f32_16x16x32_bf16 v[56:59], v[136:139], v[160:163], v[56:59]
	s_nop 0
	v_mfma_f32_16x16x32_bf16 v[56:59], v[140:143], v[164:167], v[56:59]
	s_waitcnt lgkmcnt(5)
	v_mfma_f32_16x16x32_bf16 v[52:55], v[128:131], v[168:171], v[52:55]
	s_waitcnt lgkmcnt(4)
	v_mfma_f32_16x16x32_bf16 v[52:55], v[132:135], v[172:175], v[52:55]
	v_mfma_f32_16x16x32_bf16 v[48:51], v[136:139], v[168:171], v[48:51]
	s_nop 0
	v_mfma_f32_16x16x32_bf16 v[48:51], v[140:143], v[172:175], v[48:51]
	s_waitcnt lgkmcnt(3)
	v_mfma_f32_16x16x32_bf16 v[44:47], v[128:131], v[176:179], v[44:47]
	s_waitcnt lgkmcnt(2)
	v_mfma_f32_16x16x32_bf16 v[44:47], v[132:135], v[180:183], v[44:47]
	v_mfma_f32_16x16x32_bf16 v[40:43], v[136:139], v[176:179], v[40:43]
	s_nop 0
	v_mfma_f32_16x16x32_bf16 v[40:43], v[140:143], v[180:183], v[40:43]
	s_waitcnt lgkmcnt(1)
	v_mfma_f32_16x16x32_bf16 v[36:39], v[128:131], v[184:187], v[36:39]
	s_waitcnt lgkmcnt(0)
	v_mfma_f32_16x16x32_bf16 v[36:39], v[132:135], v[188:191], v[36:39]
	v_mfma_f32_16x16x32_bf16 v[32:35], v[136:139], v[184:187], v[32:35]
	s_nop 0
	v_mfma_f32_16x16x32_bf16 v[32:35], v[140:143], v[188:191], v[32:35]
	s_setprio 0
	s_setprio 1
	v_mfma_f32_16x16x32_bf16 v[28:31], v[144:147], v[160:163], v[28:31]
	s_nop 0
	v_mfma_f32_16x16x32_bf16 v[28:31], v[148:151], v[164:167], v[28:31]
	v_mfma_f32_16x16x32_bf16 v[24:27], v[152:155], v[160:163], v[24:27]
	s_nop 0
	v_mfma_f32_16x16x32_bf16 v[24:27], v[156:159], v[164:167], v[24:27]
	v_mfma_f32_16x16x32_bf16 v[20:23], v[144:147], v[168:171], v[20:23]
	s_nop 0
	v_mfma_f32_16x16x32_bf16 v[20:23], v[148:151], v[172:175], v[20:23]
	v_mfma_f32_16x16x32_bf16 v[16:19], v[152:155], v[168:171], v[16:19]
	s_nop 0
	v_mfma_f32_16x16x32_bf16 v[16:19], v[156:159], v[172:175], v[16:19]
	v_mfma_f32_16x16x32_bf16 v[12:15], v[144:147], v[176:179], v[12:15]
	s_nop 0
	v_mfma_f32_16x16x32_bf16 v[12:15], v[148:151], v[180:183], v[12:15]
	v_mfma_f32_16x16x32_bf16 v[8:11], v[152:155], v[176:179], v[8:11]
	s_nop 0
	v_mfma_f32_16x16x32_bf16 v[8:11], v[156:159], v[180:183], v[8:11]
	v_mfma_f32_16x16x32_bf16 v[4:7], v[144:147], v[184:187], v[4:7]
	s_nop 0
	v_mfma_f32_16x16x32_bf16 v[4:7], v[148:151], v[188:191], v[4:7]
	v_mfma_f32_16x16x32_bf16 v[0:3], v[152:155], v[184:187], v[0:3]
	s_nop 0
	v_mfma_f32_16x16x32_bf16 v[0:3], v[156:159], v[188:191], v[0:3]
	s_setprio 0
	s_barrier
	ds_read_b128 v[140:143], v211
	ds_read_b128 v[144:147], v212
	ds_read_b128 v[148:151], v213
	ds_read_b128 v[152:155], v214
	ds_read_b128 v[156:159], v215
	ds_read_b128 v[136:139], v216
	ds_read_b128 v[132:135], v217
	ds_read_b128 v[128:131], v218
	ds_read_b128 v[160:163], v219 offset:32768
	ds_read_b128 v[164:167], v219 offset:33792
	ds_read_b128 v[168:171], v219 offset:34816
	ds_read_b128 v[172:175], v219 offset:35840
	ds_read_b128 v[176:179], v219 offset:36864
	ds_read_b128 v[180:183], v219 offset:37888
	ds_read_b128 v[184:187], v219 offset:38912
	ds_read_b128 v[188:191], v219 offset:39936
	s_mov_b32 m0, s69
	s_add_i32 s93, s66, 0x20000
	buffer_load_dwordx4 v196, s[8:11], s93 offen lds
	s_add_i32 s93, s66, 0x30000
	s_mov_b32 m0, s70
	s_nop 0
	buffer_load_dwordx4 v196, s[8:11], s93 offen lds
	s_waitcnt vmcnt(8)
	s_waitcnt lgkmcnt(8)
	s_barrier
	s_setprio 1
	s_waitcnt lgkmcnt(7)
	v_mfma_f32_16x16x32_bf16 v[124:127], v[140:143], v[160:163], v[124:127]
	s_waitcnt lgkmcnt(6)
	v_mfma_f32_16x16x32_bf16 v[124:127], v[144:147], v[164:167], v[124:127]
	v_mfma_f32_16x16x32_bf16 v[120:123], v[148:151], v[160:163], v[120:123]
	s_nop 0
	v_mfma_f32_16x16x32_bf16 v[120:123], v[152:155], v[164:167], v[120:123]
	s_waitcnt lgkmcnt(5)
	v_mfma_f32_16x16x32_bf16 v[116:119], v[140:143], v[168:171], v[116:119]
	s_waitcnt lgkmcnt(4)
	v_mfma_f32_16x16x32_bf16 v[116:119], v[144:147], v[172:175], v[116:119]
	v_mfma_f32_16x16x32_bf16 v[112:115], v[148:151], v[168:171], v[112:115]
	s_nop 0
	v_mfma_f32_16x16x32_bf16 v[112:115], v[152:155], v[172:175], v[112:115]
	s_waitcnt lgkmcnt(3)
	v_mfma_f32_16x16x32_bf16 v[108:111], v[140:143], v[176:179], v[108:111]
	s_waitcnt lgkmcnt(2)
	v_mfma_f32_16x16x32_bf16 v[108:111], v[144:147], v[180:183], v[108:111]
	v_mfma_f32_16x16x32_bf16 v[104:107], v[148:151], v[176:179], v[104:107]
	s_nop 0
	v_mfma_f32_16x16x32_bf16 v[104:107], v[152:155], v[180:183], v[104:107]
	s_waitcnt lgkmcnt(1)
	v_mfma_f32_16x16x32_bf16 v[100:103], v[140:143], v[184:187], v[100:103]
	s_waitcnt lgkmcnt(0)
	v_mfma_f32_16x16x32_bf16 v[100:103], v[144:147], v[188:191], v[100:103]
	v_mfma_f32_16x16x32_bf16 v[96:99], v[148:151], v[184:187], v[96:99]
	s_nop 0
	v_mfma_f32_16x16x32_bf16 v[96:99], v[152:155], v[188:191], v[96:99]
	s_setprio 0
	s_setprio 1
	v_mfma_f32_16x16x32_bf16 v[92:95], v[156:159], v[160:163], v[92:95]
	s_nop 0
	v_mfma_f32_16x16x32_bf16 v[92:95], v[136:139], v[164:167], v[92:95]
	v_mfma_f32_16x16x32_bf16 v[88:91], v[132:135], v[160:163], v[88:91]
	s_nop 0
	v_mfma_f32_16x16x32_bf16 v[88:91], v[128:131], v[164:167], v[88:91]
	v_mfma_f32_16x16x32_bf16 v[84:87], v[156:159], v[168:171], v[84:87]
	s_nop 0
	v_mfma_f32_16x16x32_bf16 v[84:87], v[136:139], v[172:175], v[84:87]
	v_mfma_f32_16x16x32_bf16 v[80:83], v[132:135], v[168:171], v[80:83]
	s_nop 0
	v_mfma_f32_16x16x32_bf16 v[80:83], v[128:131], v[172:175], v[80:83]
	v_mfma_f32_16x16x32_bf16 v[76:79], v[156:159], v[176:179], v[76:79]
	s_nop 0
	v_mfma_f32_16x16x32_bf16 v[76:79], v[136:139], v[180:183], v[76:79]
	v_mfma_f32_16x16x32_bf16 v[72:75], v[132:135], v[176:179], v[72:75]
	s_nop 0
	v_mfma_f32_16x16x32_bf16 v[72:75], v[128:131], v[180:183], v[72:75]
	v_mfma_f32_16x16x32_bf16 v[68:71], v[156:159], v[184:187], v[68:71]
	s_nop 0
	v_mfma_f32_16x16x32_bf16 v[68:71], v[136:139], v[188:191], v[68:71]
	v_mfma_f32_16x16x32_bf16 v[64:67], v[132:135], v[184:187], v[64:67]
	s_nop 0
	v_mfma_f32_16x16x32_bf16 v[64:67], v[128:131], v[188:191], v[64:67]
	s_setprio 0
	s_barrier
	ds_read_b128 v[160:163], v219 offset:49152
	ds_read_b128 v[164:167], v219 offset:50176
	ds_read_b128 v[168:171], v219 offset:51200
	ds_read_b128 v[172:175], v219 offset:52224
	ds_read_b128 v[176:179], v219 offset:53248
	ds_read_b128 v[180:183], v219 offset:54272
	ds_read_b128 v[184:187], v219 offset:55296
	ds_read_b128 v[188:191], v219 offset:56320
	s_mov_b32 m0, s73
	s_add_i32 s93, s92, 0x80
	buffer_load_dwordx4 v202, s[12:15], s93 offen lds
	s_add_i32 s93, s92, 0x80080
	s_mov_b32 m0, s74
	s_add_i32 s66, s66, 0x10080
	buffer_load_dwordx4 v202, s[12:15], s93 offen lds
	s_add_i32 s93, s92, 0x8080
	s_mov_b32 m0, s77
	s_add_i32 s92, s92, 0x88080
	buffer_load_dwordx4 v202, s[12:15], s93 offen lds
	s_mov_b32 m0, s78
	s_nop 0
	buffer_load_dwordx4 v202, s[12:15], s92 offen lds
	s_mov_b32 m0, s75
	s_nop 0
	buffer_load_dwordx4 v196, s[8:11], s67 offen lds
	s_mov_b32 m0, s76
	s_nop 0
	buffer_load_dwordx4 v196, s[8:11], s66 offen lds
	s_waitcnt vmcnt(8)
	s_waitcnt lgkmcnt(0)
	s_barrier
	s_setprio 1
	s_waitcnt lgkmcnt(7)
	v_mfma_f32_16x16x32_bf16 v[60:63], v[140:143], v[160:163], v[60:63]
	s_waitcnt lgkmcnt(6)
	v_mfma_f32_16x16x32_bf16 v[60:63], v[144:147], v[164:167], v[60:63]
	v_mfma_f32_16x16x32_bf16 v[56:59], v[148:151], v[160:163], v[56:59]
	s_nop 0
	v_mfma_f32_16x16x32_bf16 v[56:59], v[152:155], v[164:167], v[56:59]
	s_waitcnt lgkmcnt(5)
	v_mfma_f32_16x16x32_bf16 v[52:55], v[140:143], v[168:171], v[52:55]
	s_waitcnt lgkmcnt(4)
	v_mfma_f32_16x16x32_bf16 v[52:55], v[144:147], v[172:175], v[52:55]
	v_mfma_f32_16x16x32_bf16 v[48:51], v[148:151], v[168:171], v[48:51]
	s_nop 0
	v_mfma_f32_16x16x32_bf16 v[48:51], v[152:155], v[172:175], v[48:51]
	s_waitcnt lgkmcnt(3)
	v_mfma_f32_16x16x32_bf16 v[44:47], v[140:143], v[176:179], v[44:47]
	s_waitcnt lgkmcnt(2)
	v_mfma_f32_16x16x32_bf16 v[44:47], v[144:147], v[180:183], v[44:47]
	v_mfma_f32_16x16x32_bf16 v[40:43], v[148:151], v[176:179], v[40:43]
	s_nop 0
	v_mfma_f32_16x16x32_bf16 v[40:43], v[152:155], v[180:183], v[40:43]
	s_waitcnt lgkmcnt(1)
	v_mfma_f32_16x16x32_bf16 v[36:39], v[140:143], v[184:187], v[36:39]
	s_waitcnt lgkmcnt(0)
	v_mfma_f32_16x16x32_bf16 v[36:39], v[144:147], v[188:191], v[36:39]
	v_mfma_f32_16x16x32_bf16 v[32:35], v[148:151], v[184:187], v[32:35]
	s_nop 0
	v_mfma_f32_16x16x32_bf16 v[32:35], v[152:155], v[188:191], v[32:35]
	s_setprio 0
	s_setprio 1
	v_mfma_f32_16x16x32_bf16 v[28:31], v[156:159], v[160:163], v[28:31]
	s_nop 0
	v_mfma_f32_16x16x32_bf16 v[28:31], v[136:139], v[164:167], v[28:31]
	v_mfma_f32_16x16x32_bf16 v[24:27], v[132:135], v[160:163], v[24:27]
	s_nop 0
	v_mfma_f32_16x16x32_bf16 v[24:27], v[128:131], v[164:167], v[24:27]
	v_mfma_f32_16x16x32_bf16 v[20:23], v[156:159], v[168:171], v[20:23]
	s_nop 0
	v_mfma_f32_16x16x32_bf16 v[20:23], v[136:139], v[172:175], v[20:23]
	v_mfma_f32_16x16x32_bf16 v[16:19], v[132:135], v[168:171], v[16:19]
	s_nop 0
	v_mfma_f32_16x16x32_bf16 v[16:19], v[128:131], v[172:175], v[16:19]
	v_mfma_f32_16x16x32_bf16 v[12:15], v[156:159], v[176:179], v[12:15]
	s_nop 0
	v_mfma_f32_16x16x32_bf16 v[12:15], v[136:139], v[180:183], v[12:15]
	v_mfma_f32_16x16x32_bf16 v[8:11], v[132:135], v[176:179], v[8:11]
	s_nop 0
	v_mfma_f32_16x16x32_bf16 v[8:11], v[128:131], v[180:183], v[8:11]
	v_mfma_f32_16x16x32_bf16 v[4:7], v[156:159], v[184:187], v[4:7]
	s_nop 0
	v_mfma_f32_16x16x32_bf16 v[4:7], v[136:139], v[188:191], v[4:7]
	v_mfma_f32_16x16x32_bf16 v[0:3], v[132:135], v[184:187], v[0:3]
	s_nop 0
	v_mfma_f32_16x16x32_bf16 v[0:3], v[128:131], v[188:191], v[0:3]
	s_setprio 0
	s_barrier
	s_add_i32 s33, s33, 2
	s_addk_i32 s4, 0x100
	s_addk_i32 s5, 0x100
	s_cmp_gt_u32 s33, 5
	s_cbranch_scc0 .LBB0_220
	s_and_b64 vcc, exec, s[16:17]
	s_cbranch_vccz .LBB0_223
	s_barrier

.LBB0_253:
	s_waitcnt lgkmcnt(0)
	s_add_i32 s33, s91, 0x180
	s_add_i32 s42, s90, 0x180
	s_barrier
	s_setprio 1
	s_waitcnt lgkmcnt(7)
	v_mfma_f32_16x16x32_bf16 v[60:63], v[156:159], v[188:191], 0
	s_waitcnt lgkmcnt(6)
	v_mfma_f32_16x16x32_bf16 v[60:63], v[152:155], v[184:187], v[60:63]
	v_mfma_f32_16x16x32_bf16 v[56:59], v[148:151], v[188:191], 0
	s_nop 0
	v_mfma_f32_16x16x32_bf16 v[56:59], v[144:147], v[184:187], v[56:59]
	s_waitcnt lgkmcnt(5)
	v_mfma_f32_16x16x32_bf16 v[52:55], v[156:159], v[180:183], 0
	s_waitcnt lgkmcnt(4)
	v_mfma_f32_16x16x32_bf16 v[52:55], v[152:155], v[176:179], v[52:55]
	v_mfma_f32_16x16x32_bf16 v[48:51], v[148:151], v[180:183], 0
	s_nop 0
	v_mfma_f32_16x16x32_bf16 v[48:51], v[144:147], v[176:179], v[48:51]
	s_waitcnt lgkmcnt(3)
	v_mfma_f32_16x16x32_bf16 v[44:47], v[156:159], v[172:175], 0
	s_waitcnt lgkmcnt(2)
	v_mfma_f32_16x16x32_bf16 v[44:47], v[152:155], v[168:171], v[44:47]
	v_mfma_f32_16x16x32_bf16 v[40:43], v[148:151], v[172:175], 0
	s_nop 0
	v_mfma_f32_16x16x32_bf16 v[40:43], v[144:147], v[168:171], v[40:43]
	s_waitcnt lgkmcnt(1)
	v_mfma_f32_16x16x32_bf16 v[36:39], v[156:159], v[164:167], 0
	s_waitcnt lgkmcnt(0)
	v_mfma_f32_16x16x32_bf16 v[36:39], v[152:155], v[160:163], v[36:39]
	v_mfma_f32_16x16x32_bf16 v[32:35], v[148:151], v[164:167], 0
	s_nop 0
	v_mfma_f32_16x16x32_bf16 v[32:35], v[144:147], v[160:163], v[32:35]
	s_setprio 0
	s_setprio 1
	v_mfma_f32_16x16x32_bf16 v[28:31], v[140:143], v[188:191], 0
	s_nop 0
	v_mfma_f32_16x16x32_bf16 v[28:31], v[136:139], v[184:187], v[28:31]
	v_mfma_f32_16x16x32_bf16 v[24:27], v[132:135], v[188:191], 0
	s_nop 0
	v_mfma_f32_16x16x32_bf16 v[24:27], v[128:131], v[184:187], v[24:27]
	v_mfma_f32_16x16x32_bf16 v[20:23], v[140:143], v[180:183], 0
	s_nop 0
	v_mfma_f32_16x16x32_bf16 v[20:23], v[136:139], v[176:179], v[20:23]
	v_mfma_f32_16x16x32_bf16 v[16:19], v[132:135], v[180:183], 0
	s_nop 0
	v_mfma_f32_16x16x32_bf16 v[16:19], v[128:131], v[176:179], v[16:19]
	v_mfma_f32_16x16x32_bf16 v[12:15], v[140:143], v[172:175], 0
	s_nop 0
	v_mfma_f32_16x16x32_bf16 v[12:15], v[136:139], v[168:171], v[12:15]
	v_mfma_f32_16x16x32_bf16 v[8:11], v[132:135], v[172:175], 0
	s_nop 0
	v_mfma_f32_16x16x32_bf16 v[8:11], v[128:131], v[168:171], v[8:11]
	v_mfma_f32_16x16x32_bf16 v[4:7], v[140:143], v[164:167], 0
	s_nop 0
	v_mfma_f32_16x16x32_bf16 v[4:7], v[136:139], v[160:163], v[4:7]
	v_mfma_f32_16x16x32_bf16 v[0:3], v[132:135], v[164:167], 0
	s_nop 0
	v_mfma_f32_16x16x32_bf16 v[0:3], v[128:131], v[160:163], v[0:3]
	s_setprio 0
	s_barrier
	ds_read_b128 v[156:159], v203
	ds_read_b128 v[152:155], v204
	ds_read_b128 v[148:151], v205
	ds_read_b128 v[144:147], v206
	ds_read_b128 v[140:143], v207
	ds_read_b128 v[136:139], v208
	ds_read_b128 v[132:135], v209
	ds_read_b128 v[128:131], v210
	ds_read_b128 v[160:163], v197 offset:32768
	ds_read_b128 v[164:167], v197 offset:33792
	ds_read_b128 v[168:171], v197 offset:34816
	ds_read_b128 v[172:175], v197 offset:35840
	ds_read_b128 v[176:179], v197 offset:36864
	ds_read_b128 v[180:183], v197 offset:37888
	ds_read_b128 v[184:187], v197 offset:38912
	ds_read_b128 v[188:191], v197 offset:39936
	s_mov_b32 m0, s69
	s_add_i32 s10, s91, 0x20100
	buffer_load_dwordx4 v196, s[4:7], s10 offen lds
	s_add_i32 s10, s91, 0x30100
	s_mov_b32 m0, s70
	s_nop 0
	buffer_load_dwordx4 v196, s[4:7], s10 offen lds
	s_waitcnt vmcnt(8)
	s_waitcnt lgkmcnt(8)
	s_barrier
	s_setprio 1
	s_waitcnt lgkmcnt(7)
	v_mfma_f32_16x16x32_bf16 v[124:127], v[156:159], v[160:163], v[124:127]
	s_waitcnt lgkmcnt(6)
	v_mfma_f32_16x16x32_bf16 v[124:127], v[152:155], v[164:167], v[124:127]
	v_mfma_f32_16x16x32_bf16 v[120:123], v[148:151], v[160:163], v[120:123]
	s_nop 0
	v_mfma_f32_16x16x32_bf16 v[120:123], v[144:147], v[164:167], v[120:123]
	s_waitcnt lgkmcnt(5)
	v_mfma_f32_16x16x32_bf16 v[116:119], v[156:159], v[168:171], v[116:119]
	s_waitcnt lgkmcnt(4)
	v_mfma_f32_16x16x32_bf16 v[116:119], v[152:155], v[172:175], v[116:119]
	v_mfma_f32_16x16x32_bf16 v[112:115], v[148:151], v[168:171], v[112:115]
	s_nop 0
	v_mfma_f32_16x16x32_bf16 v[112:115], v[144:147], v[172:175], v[112:115]
	s_waitcnt lgkmcnt(3)
	v_mfma_f32_16x16x32_bf16 v[108:111], v[156:159], v[176:179], v[108:111]
	s_waitcnt lgkmcnt(2)
	v_mfma_f32_16x16x32_bf16 v[108:111], v[152:155], v[180:183], v[108:111]
	v_mfma_f32_16x16x32_bf16 v[104:107], v[148:151], v[176:179], v[104:107]
	s_nop 0
	v_mfma_f32_16x16x32_bf16 v[104:107], v[144:147], v[180:183], v[104:107]
	s_waitcnt lgkmcnt(1)
	v_mfma_f32_16x16x32_bf16 v[100:103], v[156:159], v[184:187], v[100:103]
	s_waitcnt lgkmcnt(0)
	v_mfma_f32_16x16x32_bf16 v[100:103], v[152:155], v[188:191], v[100:103]
	v_mfma_f32_16x16x32_bf16 v[96:99], v[148:151], v[184:187], v[96:99]
	s_nop 0
	v_mfma_f32_16x16x32_bf16 v[96:99], v[144:147], v[188:191], v[96:99]
	s_setprio 0
	s_setprio 1
	v_mfma_f32_16x16x32_bf16 v[92:95], v[140:143], v[160:163], v[92:95]
	s_nop 0
	v_mfma_f32_16x16x32_bf16 v[92:95], v[136:139], v[164:167], v[92:95]
	v_mfma_f32_16x16x32_bf16 v[88:91], v[132:135], v[160:163], v[88:91]
	s_nop 0
	v_mfma_f32_16x16x32_bf16 v[88:91], v[128:131], v[164:167], v[88:91]
	v_mfma_f32_16x16x32_bf16 v[84:87], v[140:143], v[168:171], v[84:87]
	s_nop 0
	v_mfma_f32_16x16x32_bf16 v[84:87], v[136:139], v[172:175], v[84:87]
	v_mfma_f32_16x16x32_bf16 v[80:83], v[132:135], v[168:171], v[80:83]
	s_nop 0
	v_mfma_f32_16x16x32_bf16 v[80:83], v[128:131], v[172:175], v[80:83]
	v_mfma_f32_16x16x32_bf16 v[76:79], v[140:143], v[176:179], v[76:79]
	s_nop 0
	v_mfma_f32_16x16x32_bf16 v[76:79], v[136:139], v[180:183], v[76:79]
	v_mfma_f32_16x16x32_bf16 v[72:75], v[132:135], v[176:179], v[72:75]
	s_nop 0
	v_mfma_f32_16x16x32_bf16 v[72:75], v[128:131], v[180:183], v[72:75]
	v_mfma_f32_16x16x32_bf16 v[68:71], v[140:143], v[184:187], v[68:71]
	s_nop 0
	v_mfma_f32_16x16x32_bf16 v[68:71], v[136:139], v[188:191], v[68:71]
	v_mfma_f32_16x16x32_bf16 v[64:67], v[132:135], v[184:187], v[64:67]
	s_nop 0
	v_mfma_f32_16x16x32_bf16 v[64:67], v[128:131], v[188:191], v[64:67]
	s_setprio 0
	s_barrier
	ds_read_b128 v[160:163], v197 offset:49152
	ds_read_b128 v[164:167], v197 offset:50176
	ds_read_b128 v[168:171], v197 offset:51200
	ds_read_b128 v[172:175], v197 offset:52224
	ds_read_b128 v[176:179], v197 offset:53248
	ds_read_b128 v[180:183], v197 offset:54272
	ds_read_b128 v[184:187], v197 offset:55296
	ds_read_b128 v[188:191], v197 offset:56320
	s_mov_b32 m0, s72
	s_mov_b32 s10, s6
	s_mov_b32 s11, s7
	buffer_load_dwordx4 v192, s[8:11], s42 offen lds
	s_add_i32 s42, s90, 0x20180
	s_mov_b32 m0, s73
	s_nop 0
	buffer_load_dwordx4 v192, s[8:11], s42 offen lds
	s_add_i32 s42, s90, 0x2180
	s_mov_b32 m0, s76
	s_nop 0
	buffer_load_dwordx4 v192, s[8:11], s42 offen lds
	s_add_i32 s42, s90, 0x22180
	s_mov_b32 m0, s77
	s_nop 0
	buffer_load_dwordx4 v192, s[8:11], s42 offen lds
	s_mov_b32 m0, s74
	s_nop 0
	buffer_load_dwordx4 v196, s[4:7], s33 offen lds
	s_add_i32 s33, s91, 0x10180
	s_mov_b32 m0, s75
	s_nop 0
	buffer_load_dwordx4 v196, s[4:7], s33 offen lds
	s_waitcnt vmcnt(8)
	s_waitcnt lgkmcnt(0)
	s_barrier
	s_setprio 1
	s_waitcnt lgkmcnt(7)
	v_mfma_f32_16x16x32_bf16 v[60:63], v[156:159], v[160:163], v[60:63]
	s_waitcnt lgkmcnt(6)
	v_mfma_f32_16x16x32_bf16 v[60:63], v[152:155], v[164:167], v[60:63]
	v_mfma_f32_16x16x32_bf16 v[56:59], v[148:151], v[160:163], v[56:59]
	s_nop 0
	v_mfma_f32_16x16x32_bf16 v[56:59], v[144:147], v[164:167], v[56:59]
	s_waitcnt lgkmcnt(5)
	v_mfma_f32_16x16x32_bf16 v[52:55], v[156:159], v[168:171], v[52:55]
	s_waitcnt lgkmcnt(4)
	v_mfma_f32_16x16x32_bf16 v[52:55], v[152:155], v[172:175], v[52:55]
	v_mfma_f32_16x16x32_bf16 v[48:51], v[148:151], v[168:171], v[48:51]
	s_nop 0
	v_mfma_f32_16x16x32_bf16 v[48:51], v[144:147], v[172:175], v[48:51]
	s_waitcnt lgkmcnt(3)
	v_mfma_f32_16x16x32_bf16 v[44:47], v[156:159], v[176:179], v[44:47]
	s_waitcnt lgkmcnt(2)
	v_mfma_f32_16x16x32_bf16 v[44:47], v[152:155], v[180:183], v[44:47]
	v_mfma_f32_16x16x32_bf16 v[40:43], v[148:151], v[176:179], v[40:43]
	s_nop 0
	v_mfma_f32_16x16x32_bf16 v[40:43], v[144:147], v[180:183], v[40:43]
	s_waitcnt lgkmcnt(1)
	v_mfma_f32_16x16x32_bf16 v[36:39], v[156:159], v[184:187], v[36:39]
	s_waitcnt lgkmcnt(0)
	v_mfma_f32_16x16x32_bf16 v[36:39], v[152:155], v[188:191], v[36:39]
	v_mfma_f32_16x16x32_bf16 v[32:35], v[148:151], v[184:187], v[32:35]
	s_nop 0
	v_mfma_f32_16x16x32_bf16 v[32:35], v[144:147], v[188:191], v[32:35]
	s_setprio 0
	s_setprio 1
	v_mfma_f32_16x16x32_bf16 v[28:31], v[140:143], v[160:163], v[28:31]
	s_nop 0
	v_mfma_f32_16x16x32_bf16 v[28:31], v[136:139], v[164:167], v[28:31]
	v_mfma_f32_16x16x32_bf16 v[24:27], v[132:135], v[160:163], v[24:27]
	s_nop 0
	v_mfma_f32_16x16x32_bf16 v[24:27], v[128:131], v[164:167], v[24:27]
	v_mfma_f32_16x16x32_bf16 v[20:23], v[140:143], v[168:171], v[20:23]
	s_nop 0
	v_mfma_f32_16x16x32_bf16 v[20:23], v[136:139], v[172:175], v[20:23]
	v_mfma_f32_16x16x32_bf16 v[16:19], v[132:135], v[168:171], v[16:19]
	s_nop 0
	v_mfma_f32_16x16x32_bf16 v[16:19], v[128:131], v[172:175], v[16:19]
	v_mfma_f32_16x16x32_bf16 v[12:15], v[140:143], v[176:179], v[12:15]
	s_nop 0
	v_mfma_f32_16x16x32_bf16 v[12:15], v[136:139], v[180:183], v[12:15]
	v_mfma_f32_16x16x32_bf16 v[8:11], v[132:135], v[176:179], v[8:11]
	s_nop 0
	v_mfma_f32_16x16x32_bf16 v[8:11], v[128:131], v[180:183], v[8:11]
	v_mfma_f32_16x16x32_bf16 v[4:7], v[140:143], v[184:187], v[4:7]
	s_nop 0
	v_mfma_f32_16x16x32_bf16 v[4:7], v[136:139], v[188:191], v[4:7]
	v_mfma_f32_16x16x32_bf16 v[0:3], v[132:135], v[184:187], v[0:3]
	s_nop 0
	v_mfma_f32_16x16x32_bf16 v[0:3], v[128:131], v[188:191], v[0:3]
	s_setprio 0
	s_barrier
	s_add_i32 s33, s91, 0x30180
	s_add_i32 s42, s90, 0x200
	s_mov_b32 s43, 0
.LBB0_254:
	ds_read_b128 v[128:131], v193
	ds_read_b128 v[132:135], v194
	ds_read_b128 v[136:139], v195
	ds_read_b128 v[140:143], v198
	ds_read_b128 v[144:147], v199
	ds_read_b128 v[148:151], v200
	ds_read_b128 v[152:155], v201
	ds_read_b128 v[156:159], v202
	ds_read_b128 v[160:163], v197
	ds_read_b128 v[164:167], v197 offset:1024
	ds_read_b128 v[168:171], v197 offset:2048
	ds_read_b128 v[172:175], v197 offset:3072
	ds_read_b128 v[176:179], v197 offset:4096
	ds_read_b128 v[180:183], v197 offset:5120
	ds_read_b128 v[184:187], v197 offset:6144
	ds_read_b128 v[188:191], v197 offset:7168
	s_add_i32 s66, s33, 0xfffd0080
	s_cmp_eq_u32 s43, 4
	s_cselect_b32 s66, s88, s66
	s_cselect_b32 s90, s89, s42
	s_add_i32 s67, s66, 0x80
	s_mov_b32 m0, s78
	s_add_i32 s91, s33, 0xffff0000
	buffer_load_dwordx4 v196, s[4:7], s91 offen lds
	s_mov_b32 m0, s79
	s_nop 0
	buffer_load_dwordx4 v196, s[4:7], s33 offen lds
	s_waitcnt vmcnt(8)
	s_waitcnt lgkmcnt(8)
	s_barrier
	s_setprio 1
	s_waitcnt lgkmcnt(7)
	v_mfma_f32_16x16x32_bf16 v[124:127], v[128:131], v[160:163], v[124:127]
	s_waitcnt lgkmcnt(6)
	v_mfma_f32_16x16x32_bf16 v[124:127], v[132:135], v[164:167], v[124:127]
	v_mfma_f32_16x16x32_bf16 v[120:123], v[136:139], v[160:163], v[120:123]
	s_nop 0
	v_mfma_f32_16x16x32_bf16 v[120:123], v[140:143], v[164:167], v[120:123]
	s_waitcnt lgkmcnt(5)
	v_mfma_f32_16x16x32_bf16 v[116:119], v[128:131], v[168:171], v[116:119]
	s_waitcnt lgkmcnt(4)
	v_mfma_f32_16x16x32_bf16 v[116:119], v[132:135], v[172:175], v[116:119]
	v_mfma_f32_16x16x32_bf16 v[112:115], v[136:139], v[168:171], v[112:115]
	s_nop 0
	v_mfma_f32_16x16x32_bf16 v[112:115], v[140:143], v[172:175], v[112:115]
	s_waitcnt lgkmcnt(3)
	v_mfma_f32_16x16x32_bf16 v[108:111], v[128:131], v[176:179], v[108:111]
	s_waitcnt lgkmcnt(2)
	v_mfma_f32_16x16x32_bf16 v[108:111], v[132:135], v[180:183], v[108:111]
	v_mfma_f32_16x16x32_bf16 v[104:107], v[136:139], v[176:179], v[104:107]
	s_nop 0
	v_mfma_f32_16x16x32_bf16 v[104:107], v[140:143], v[180:183], v[104:107]
	s_waitcnt lgkmcnt(1)
	v_mfma_f32_16x16x32_bf16 v[100:103], v[128:131], v[184:187], v[100:103]
	s_waitcnt lgkmcnt(0)
	v_mfma_f32_16x16x32_bf16 v[100:103], v[132:135], v[188:191], v[100:103]
	v_mfma_f32_16x16x32_bf16 v[96:99], v[136:139], v[184:187], v[96:99]
	s_nop 0
	v_mfma_f32_16x16x32_bf16 v[96:99], v[140:143], v[188:191], v[96:99]
	s_setprio 0
	s_setprio 1
	v_mfma_f32_16x16x32_bf16 v[92:95], v[144:147], v[160:163], v[92:95]
	s_nop 0
	v_mfma_f32_16x16x32_bf16 v[92:95], v[148:151], v[164:167], v[92:95]
	v_mfma_f32_16x16x32_bf16 v[88:91], v[152:155], v[160:163], v[88:91]
	s_nop 0
	v_mfma_f32_16x16x32_bf16 v[88:91], v[156:159], v[164:167], v[88:91]
	v_mfma_f32_16x16x32_bf16 v[84:87], v[144:147], v[168:171], v[84:87]
	s_nop 0
	v_mfma_f32_16x16x32_bf16 v[84:87], v[148:151], v[172:175], v[84:87]
	v_mfma_f32_16x16x32_bf16 v[80:83], v[152:155], v[168:171], v[80:83]
	s_nop 0
	v_mfma_f32_16x16x32_bf16 v[80:83], v[156:159], v[172:175], v[80:83]
	v_mfma_f32_16x16x32_bf16 v[76:79], v[144:147], v[176:179], v[76:79]
	s_nop 0
	v_mfma_f32_16x16x32_bf16 v[76:79], v[148:151], v[180:183], v[76:79]
	v_mfma_f32_16x16x32_bf16 v[72:75], v[152:155], v[176:179], v[72:75]
	s_nop 0
	v_mfma_f32_16x16x32_bf16 v[72:75], v[156:159], v[180:183], v[72:75]
	v_mfma_f32_16x16x32_bf16 v[68:71], v[144:147], v[184:187], v[68:71]
	s_nop 0
	v_mfma_f32_16x16x32_bf16 v[68:71], v[148:151], v[188:191], v[68:71]
	v_mfma_f32_16x16x32_bf16 v[64:67], v[152:155], v[184:187], v[64:67]
	s_nop 0
	v_mfma_f32_16x16x32_bf16 v[64:67], v[156:159], v[188:191], v[64:67]
	s_setprio 0
	s_barrier
	ds_read_b128 v[160:163], v197 offset:16384
	ds_read_b128 v[164:167], v197 offset:17408
	ds_read_b128 v[168:171], v197 offset:18432
	ds_read_b128 v[172:175], v197 offset:19456
	ds_read_b128 v[176:179], v197 offset:20480
	ds_read_b128 v[180:183], v197 offset:21504
	ds_read_b128 v[184:187], v197 offset:22528
	ds_read_b128 v[188:191], v197 offset:23552
	s_mov_b32 m0, s62
	s_add_i32 s91, s90, 0x20000
	buffer_load_dwordx4 v192, s[8:11], s90 offen lds
	s_mov_b32 m0, s63
	s_nop 0
	buffer_load_dwordx4 v192, s[8:11], s91 offen lds
	s_add_i32 s91, s90, 0x2000
	s_mov_b32 m0, s64
	s_nop 0
	buffer_load_dwordx4 v192, s[8:11], s91 offen lds
	s_add_i32 s91, s90, 0x22000
	s_mov_b32 m0, s65
	s_nop 0
	buffer_load_dwordx4 v192, s[8:11], s91 offen lds
	s_mov_b32 m0, s47
	s_add_i32 s91, s66, 0x10000
	buffer_load_dwordx4 v196, s[4:7], s66 offen lds
	s_mov_b32 m0, s68
	s_nop 0
	buffer_load_dwordx4 v196, s[4:7], s91 offen lds
	s_waitcnt vmcnt(8)
	s_waitcnt lgkmcnt(0)
	s_barrier
	s_setprio 1
	s_waitcnt lgkmcnt(7)
	v_mfma_f32_16x16x32_bf16 v[60:63], v[128:131], v[160:163], v[60:63]
	s_waitcnt lgkmcnt(6)
	v_mfma_f32_16x16x32_bf16 v[60:63], v[132:135], v[164:167], v[60:63]
	v_mfma_f32_16x16x32_bf16 v[56:59], v[136:139], v[160:163], v[56:59]
	s_nop 0
	v_mfma_f32_16x16x32_bf16 v[56:59], v[140:143], v[164:167], v[56:59]
	s_waitcnt lgkmcnt(5)
	v_mfma_f32_16x16x32_bf16 v[52:55], v[128:131], v[168:171], v[52:55]
	s_waitcnt lgkmcnt(4)
	v_mfma_f32_16x16x32_bf16 v[52:55], v[132:135], v[172:175], v[52:55]
	v_mfma_f32_16x16x32_bf16 v[48:51], v[136:139], v[168:171], v[48:51]
	s_nop 0
	v_mfma_f32_16x16x32_bf16 v[48:51], v[140:143], v[172:175], v[48:51]
	s_waitcnt lgkmcnt(3)
	v_mfma_f32_16x16x32_bf16 v[44:47], v[128:131], v[176:179], v[44:47]
	s_waitcnt lgkmcnt(2)
	v_mfma_f32_16x16x32_bf16 v[44:47], v[132:135], v[180:183], v[44:47]
	v_mfma_f32_16x16x32_bf16 v[40:43], v[136:139], v[176:179], v[40:43]
	s_nop 0
	v_mfma_f32_16x16x32_bf16 v[40:43], v[140:143], v[180:183], v[40:43]
	s_waitcnt lgkmcnt(1)
	v_mfma_f32_16x16x32_bf16 v[36:39], v[128:131], v[184:187], v[36:39]
	s_waitcnt lgkmcnt(0)
	v_mfma_f32_16x16x32_bf16 v[36:39], v[132:135], v[188:191], v[36:39]
	v_mfma_f32_16x16x32_bf16 v[32:35], v[136:139], v[184:187], v[32:35]
	s_nop 0
	v_mfma_f32_16x16x32_bf16 v[32:35], v[140:143], v[188:191], v[32:35]
	s_setprio 0
	s_setprio 1
	v_mfma_f32_16x16x32_bf16 v[28:31], v[144:147], v[160:163], v[28:31]
	s_nop 0
	v_mfma_f32_16x16x32_bf16 v[28:31], v[148:151], v[164:167], v[28:31]
	v_mfma_f32_16x16x32_bf16 v[24:27], v[152:155], v[160:163], v[24:27]
	s_nop 0
	v_mfma_f32_16x16x32_bf16 v[24:27], v[156:159], v[164:167], v[24:27]
	v_mfma_f32_16x16x32_bf16 v[20:23], v[144:147], v[168:171], v[20:23]
	s_nop 0
	v_mfma_f32_16x16x32_bf16 v[20:23], v[148:151], v[172:175], v[20:23]
	v_mfma_f32_16x16x32_bf16 v[16:19], v[152:155], v[168:171], v[16:19]
	s_nop 0
	v_mfma_f32_16x16x32_bf16 v[16:19], v[156:159], v[172:175], v[16:19]
	v_mfma_f32_16x16x32_bf16 v[12:15], v[144:147], v[176:179], v[12:15]
	s_nop 0
	v_mfma_f32_16x16x32_bf16 v[12:15], v[148:151], v[180:183], v[12:15]
	v_mfma_f32_16x16x32_bf16 v[8:11], v[152:155], v[176:179], v[8:11]
	s_nop 0
	v_mfma_f32_16x16x32_bf16 v[8:11], v[156:159], v[180:183], v[8:11]
	v_mfma_f32_16x16x32_bf16 v[4:7], v[144:147], v[184:187], v[4:7]
	s_nop 0
	v_mfma_f32_16x16x32_bf16 v[4:7], v[148:151], v[188:191], v[4:7]
	v_mfma_f32_16x16x32_bf16 v[0:3], v[152:155], v[184:187], v[0:3]
	s_nop 0
	v_mfma_f32_16x16x32_bf16 v[0:3], v[156:159], v[188:191], v[0:3]
	s_setprio 0
	s_barrier
	ds_read_b128 v[140:143], v203
	ds_read_b128 v[144:147], v204
	ds_read_b128 v[148:151], v205
	ds_read_b128 v[152:155], v206
	ds_read_b128 v[156:159], v207
	ds_read_b128 v[136:139], v208
	ds_read_b128 v[132:135], v209
	ds_read_b128 v[128:131], v210
	ds_read_b128 v[160:163], v197 offset:32768
	ds_read_b128 v[164:167], v197 offset:33792
	ds_read_b128 v[168:171], v197 offset:34816
	ds_read_b128 v[172:175], v197 offset:35840
	ds_read_b128 v[176:179], v197 offset:36864
	ds_read_b128 v[180:183], v197 offset:37888
	ds_read_b128 v[184:187], v197 offset:38912
	ds_read_b128 v[188:191], v197 offset:39936
	s_mov_b32 m0, s69
	s_add_i32 s91, s66, 0x20000
	buffer_load_dwordx4 v196, s[4:7], s91 offen lds
	s_add_i32 s91, s66, 0x30000
	s_mov_b32 m0, s70
	s_nop 0
	buffer_load_dwordx4 v196, s[4:7], s91 offen lds
	s_waitcnt vmcnt(8)
	s_waitcnt lgkmcnt(8)
	s_barrier
	s_setprio 1
	s_waitcnt lgkmcnt(7)
	v_mfma_f32_16x16x32_bf16 v[124:127], v[140:143], v[160:163], v[124:127]
	s_waitcnt lgkmcnt(6)
	v_mfma_f32_16x16x32_bf16 v[124:127], v[144:147], v[164:167], v[124:127]
	v_mfma_f32_16x16x32_bf16 v[120:123], v[148:151], v[160:163], v[120:123]
	s_nop 0
	v_mfma_f32_16x16x32_bf16 v[120:123], v[152:155], v[164:167], v[120:123]
	s_waitcnt lgkmcnt(5)
	v_mfma_f32_16x16x32_bf16 v[116:119], v[140:143], v[168:171], v[116:119]
	s_waitcnt lgkmcnt(4)
	v_mfma_f32_16x16x32_bf16 v[116:119], v[144:147], v[172:175], v[116:119]
	v_mfma_f32_16x16x32_bf16 v[112:115], v[148:151], v[168:171], v[112:115]
	s_nop 0
	v_mfma_f32_16x16x32_bf16 v[112:115], v[152:155], v[172:175], v[112:115]
	s_waitcnt lgkmcnt(3)
	v_mfma_f32_16x16x32_bf16 v[108:111], v[140:143], v[176:179], v[108:111]
	s_waitcnt lgkmcnt(2)
	v_mfma_f32_16x16x32_bf16 v[108:111], v[144:147], v[180:183], v[108:111]
	v_mfma_f32_16x16x32_bf16 v[104:107], v[148:151], v[176:179], v[104:107]
	s_nop 0
	v_mfma_f32_16x16x32_bf16 v[104:107], v[152:155], v[180:183], v[104:107]
	s_waitcnt lgkmcnt(1)
	v_mfma_f32_16x16x32_bf16 v[100:103], v[140:143], v[184:187], v[100:103]
	s_waitcnt lgkmcnt(0)
	v_mfma_f32_16x16x32_bf16 v[100:103], v[144:147], v[188:191], v[100:103]
	v_mfma_f32_16x16x32_bf16 v[96:99], v[148:151], v[184:187], v[96:99]
	s_nop 0
	v_mfma_f32_16x16x32_bf16 v[96:99], v[152:155], v[188:191], v[96:99]
	s_setprio 0
	s_setprio 1
	v_mfma_f32_16x16x32_bf16 v[92:95], v[156:159], v[160:163], v[92:95]
	s_nop 0
	v_mfma_f32_16x16x32_bf16 v[92:95], v[136:139], v[164:167], v[92:95]
	v_mfma_f32_16x16x32_bf16 v[88:91], v[132:135], v[160:163], v[88:91]
	s_nop 0
	v_mfma_f32_16x16x32_bf16 v[88:91], v[128:131], v[164:167], v[88:91]
	v_mfma_f32_16x16x32_bf16 v[84:87], v[156:159], v[168:171], v[84:87]
	s_nop 0
	v_mfma_f32_16x16x32_bf16 v[84:87], v[136:139], v[172:175], v[84:87]
	v_mfma_f32_16x16x32_bf16 v[80:83], v[132:135], v[168:171], v[80:83]
	s_nop 0
	v_mfma_f32_16x16x32_bf16 v[80:83], v[128:131], v[172:175], v[80:83]
	v_mfma_f32_16x16x32_bf16 v[76:79], v[156:159], v[176:179], v[76:79]
	s_nop 0
	v_mfma_f32_16x16x32_bf16 v[76:79], v[136:139], v[180:183], v[76:79]
	v_mfma_f32_16x16x32_bf16 v[72:75], v[132:135], v[176:179], v[72:75]
	s_nop 0
	v_mfma_f32_16x16x32_bf16 v[72:75], v[128:131], v[180:183], v[72:75]
	v_mfma_f32_16x16x32_bf16 v[68:71], v[156:159], v[184:187], v[68:71]
	s_nop 0
	v_mfma_f32_16x16x32_bf16 v[68:71], v[136:139], v[188:191], v[68:71]
	v_mfma_f32_16x16x32_bf16 v[64:67], v[132:135], v[184:187], v[64:67]
	s_nop 0
	v_mfma_f32_16x16x32_bf16 v[64:67], v[128:131], v[188:191], v[64:67]
	s_setprio 0
	s_barrier
	ds_read_b128 v[160:163], v197 offset:49152
	ds_read_b128 v[164:167], v197 offset:50176
	ds_read_b128 v[168:171], v197 offset:51200
	ds_read_b128 v[172:175], v197 offset:52224
	ds_read_b128 v[176:179], v197 offset:53248
	ds_read_b128 v[180:183], v197 offset:54272
	ds_read_b128 v[184:187], v197 offset:55296
	ds_read_b128 v[188:191], v197 offset:56320
	s_mov_b32 m0, s72
	s_add_i32 s91, s90, 0x80
	buffer_load_dwordx4 v192, s[8:11], s91 offen lds
	s_add_i32 s91, s90, 0x20080
	s_mov_b32 m0, s73
	s_add_i32 s66, s66, 0x10080
	buffer_load_dwordx4 v192, s[8:11], s91 offen lds
	s_add_i32 s91, s90, 0x2080
	s_mov_b32 m0, s76
	s_add_i32 s90, s90, 0x22080
	buffer_load_dwordx4 v192, s[8:11], s91 offen lds
	s_mov_b32 m0, s77
	s_nop 0
	buffer_load_dwordx4 v192, s[8:11], s90 offen lds
	s_mov_b32 m0, s74
	s_nop 0
	buffer_load_dwordx4 v196, s[4:7], s67 offen lds
	s_mov_b32 m0, s75
	s_nop 0
	buffer_load_dwordx4 v196, s[4:7], s66 offen lds
	s_waitcnt vmcnt(8)
	s_waitcnt lgkmcnt(0)
	s_barrier
	s_setprio 1
	s_waitcnt lgkmcnt(7)
	v_mfma_f32_16x16x32_bf16 v[60:63], v[140:143], v[160:163], v[60:63]
	s_waitcnt lgkmcnt(6)
	v_mfma_f32_16x16x32_bf16 v[60:63], v[144:147], v[164:167], v[60:63]
	v_mfma_f32_16x16x32_bf16 v[56:59], v[148:151], v[160:163], v[56:59]
	s_nop 0
	v_mfma_f32_16x16x32_bf16 v[56:59], v[152:155], v[164:167], v[56:59]
	s_waitcnt lgkmcnt(5)
	v_mfma_f32_16x16x32_bf16 v[52:55], v[140:143], v[168:171], v[52:55]
	s_waitcnt lgkmcnt(4)
	v_mfma_f32_16x16x32_bf16 v[52:55], v[144:147], v[172:175], v[52:55]
	v_mfma_f32_16x16x32_bf16 v[48:51], v[148:151], v[168:171], v[48:51]
	s_nop 0
	v_mfma_f32_16x16x32_bf16 v[48:51], v[152:155], v[172:175], v[48:51]
	s_waitcnt lgkmcnt(3)
	v_mfma_f32_16x16x32_bf16 v[44:47], v[140:143], v[176:179], v[44:47]
	s_waitcnt lgkmcnt(2)
	v_mfma_f32_16x16x32_bf16 v[44:47], v[144:147], v[180:183], v[44:47]
	v_mfma_f32_16x16x32_bf16 v[40:43], v[148:151], v[176:179], v[40:43]
	s_nop 0
	v_mfma_f32_16x16x32_bf16 v[40:43], v[152:155], v[180:183], v[40:43]
	s_waitcnt lgkmcnt(1)
	v_mfma_f32_16x16x32_bf16 v[36:39], v[140:143], v[184:187], v[36:39]
	s_waitcnt lgkmcnt(0)
	v_mfma_f32_16x16x32_bf16 v[36:39], v[144:147], v[188:191], v[36:39]
	v_mfma_f32_16x16x32_bf16 v[32:35], v[148:151], v[184:187], v[32:35]
	s_nop 0
	v_mfma_f32_16x16x32_bf16 v[32:35], v[152:155], v[188:191], v[32:35]
	s_setprio 0
	s_setprio 1
	v_mfma_f32_16x16x32_bf16 v[28:31], v[156:159], v[160:163], v[28:31]
	s_nop 0
	v_mfma_f32_16x16x32_bf16 v[28:31], v[136:139], v[164:167], v[28:31]
	v_mfma_f32_16x16x32_bf16 v[24:27], v[132:135], v[160:163], v[24:27]
	s_nop 0
	v_mfma_f32_16x16x32_bf16 v[24:27], v[128:131], v[164:167], v[24:27]
	v_mfma_f32_16x16x32_bf16 v[20:23], v[156:159], v[168:171], v[20:23]
	s_nop 0
	v_mfma_f32_16x16x32_bf16 v[20:23], v[136:139], v[172:175], v[20:23]
	v_mfma_f32_16x16x32_bf16 v[16:19], v[132:135], v[168:171], v[16:19]
	s_nop 0
	v_mfma_f32_16x16x32_bf16 v[16:19], v[128:131], v[172:175], v[16:19]
	v_mfma_f32_16x16x32_bf16 v[12:15], v[156:159], v[176:179], v[12:15]
	s_nop 0
	v_mfma_f32_16x16x32_bf16 v[12:15], v[136:139], v[180:183], v[12:15]
	v_mfma_f32_16x16x32_bf16 v[8:11], v[132:135], v[176:179], v[8:11]
	s_nop 0
	v_mfma_f32_16x16x32_bf16 v[8:11], v[128:131], v[180:183], v[8:11]
	v_mfma_f32_16x16x32_bf16 v[4:7], v[156:159], v[184:187], v[4:7]
	s_nop 0
	v_mfma_f32_16x16x32_bf16 v[4:7], v[136:139], v[188:191], v[4:7]
	v_mfma_f32_16x16x32_bf16 v[0:3], v[132:135], v[184:187], v[0:3]
	s_nop 0
	v_mfma_f32_16x16x32_bf16 v[0:3], v[128:131], v[188:191], v[0:3]
	s_setprio 0
	s_barrier
	s_add_i32 s43, s43, 2
	s_addk_i32 s33, 0x100
	s_addk_i32 s42, 0x100
	s_cmp_gt_u32 s43, 5
	s_cbranch_scc0 .LBB0_254
	s_and_b64 vcc, exec, s[14:15]
	s_cbranch_vccz .LBB0_257
	s_barrier

.LBB0_344:
	s_waitcnt lgkmcnt(0)
	s_add_i32 s4, s60, 0x180
	s_add_i32 s5, s36, 0x180
	s_barrier
	s_setprio 1
	s_waitcnt lgkmcnt(7)
	v_mfma_f32_16x16x32_bf16 v[60:63], v[164:167], v[196:199], 0
	s_waitcnt lgkmcnt(6)
	v_mfma_f32_16x16x32_bf16 v[60:63], v[160:163], v[192:195], v[60:63]
	v_mfma_f32_16x16x32_bf16 v[56:59], v[156:159], v[196:199], 0
	s_nop 0
	v_mfma_f32_16x16x32_bf16 v[56:59], v[152:155], v[192:195], v[56:59]
	s_waitcnt lgkmcnt(5)
	v_mfma_f32_16x16x32_bf16 v[52:55], v[164:167], v[188:191], 0
	s_waitcnt lgkmcnt(4)
	v_mfma_f32_16x16x32_bf16 v[52:55], v[160:163], v[184:187], v[52:55]
	v_mfma_f32_16x16x32_bf16 v[48:51], v[156:159], v[188:191], 0
	s_nop 0
	v_mfma_f32_16x16x32_bf16 v[48:51], v[152:155], v[184:187], v[48:51]
	s_waitcnt lgkmcnt(3)
	v_mfma_f32_16x16x32_bf16 v[44:47], v[164:167], v[180:183], 0
	s_waitcnt lgkmcnt(2)
	v_mfma_f32_16x16x32_bf16 v[44:47], v[160:163], v[176:179], v[44:47]
	v_mfma_f32_16x16x32_bf16 v[40:43], v[156:159], v[180:183], 0
	s_nop 0
	v_mfma_f32_16x16x32_bf16 v[40:43], v[152:155], v[176:179], v[40:43]
	s_waitcnt lgkmcnt(1)
	v_mfma_f32_16x16x32_bf16 v[36:39], v[164:167], v[172:175], 0
	s_waitcnt lgkmcnt(0)
	v_mfma_f32_16x16x32_bf16 v[36:39], v[160:163], v[168:171], v[36:39]
	v_mfma_f32_16x16x32_bf16 v[32:35], v[156:159], v[172:175], 0
	s_nop 0
	v_mfma_f32_16x16x32_bf16 v[32:35], v[152:155], v[168:171], v[32:35]
	s_setprio 0
	s_setprio 1
	v_mfma_f32_16x16x32_bf16 v[28:31], v[148:151], v[196:199], 0
	s_nop 0
	v_mfma_f32_16x16x32_bf16 v[28:31], v[144:147], v[192:195], v[28:31]
	v_mfma_f32_16x16x32_bf16 v[24:27], v[140:143], v[196:199], 0
	s_nop 0
	v_mfma_f32_16x16x32_bf16 v[24:27], v[136:139], v[192:195], v[24:27]
	v_mfma_f32_16x16x32_bf16 v[20:23], v[148:151], v[188:191], 0
	s_nop 0
	v_mfma_f32_16x16x32_bf16 v[20:23], v[144:147], v[184:187], v[20:23]
	v_mfma_f32_16x16x32_bf16 v[16:19], v[140:143], v[188:191], 0
	s_nop 0
	v_mfma_f32_16x16x32_bf16 v[16:19], v[136:139], v[184:187], v[16:19]
	v_mfma_f32_16x16x32_bf16 v[12:15], v[148:151], v[180:183], 0
	s_nop 0
	v_mfma_f32_16x16x32_bf16 v[12:15], v[144:147], v[176:179], v[12:15]
	v_mfma_f32_16x16x32_bf16 v[8:11], v[140:143], v[180:183], 0
	s_nop 0
	v_mfma_f32_16x16x32_bf16 v[8:11], v[136:139], v[176:179], v[8:11]
	v_mfma_f32_16x16x32_bf16 v[4:7], v[148:151], v[172:175], 0
	s_nop 0
	v_mfma_f32_16x16x32_bf16 v[4:7], v[144:147], v[168:171], v[4:7]
	v_mfma_f32_16x16x32_bf16 v[0:3], v[140:143], v[172:175], 0
	s_nop 0
	v_mfma_f32_16x16x32_bf16 v[0:3], v[136:139], v[168:171], v[0:3]
	s_setprio 0
	s_barrier
	ds_read_b128 v[164:167], v225
	ds_read_b128 v[160:163], v226
	ds_read_b128 v[156:159], v227
	ds_read_b128 v[152:155], v228
	ds_read_b128 v[148:151], v229
	ds_read_b128 v[144:147], v230
	ds_read_b128 v[140:143], v231
	ds_read_b128 v[136:139], v232
	ds_read_b128 v[168:171], v233 offset:32768
	ds_read_b128 v[172:175], v233 offset:33792
	ds_read_b128 v[176:179], v233 offset:34816
	ds_read_b128 v[180:183], v233 offset:35840
	ds_read_b128 v[184:187], v233 offset:36864
	ds_read_b128 v[188:191], v233 offset:37888
	ds_read_b128 v[192:195], v233 offset:38912
	ds_read_b128 v[196:199], v233 offset:39936
	s_mov_b32 m0, s72
	s_add_i32 s14, s60, 0x100100
	buffer_load_dwordx4 v214, s[8:11], s14 offen lds
	s_add_i32 s14, s60, 0x180100
	s_mov_b32 m0, s73
	s_nop 0
	buffer_load_dwordx4 v214, s[8:11], s14 offen lds
	s_waitcnt vmcnt(10)
	s_waitcnt lgkmcnt(8)
	s_barrier
	s_setprio 1
	s_waitcnt lgkmcnt(7)
	v_mfma_f32_16x16x32_bf16 v[124:127], v[164:167], v[168:171], v[124:127]
	s_waitcnt lgkmcnt(6)
	v_mfma_f32_16x16x32_bf16 v[124:127], v[160:163], v[172:175], v[124:127]
	v_mfma_f32_16x16x32_bf16 v[120:123], v[156:159], v[168:171], v[120:123]
	s_nop 0
	v_mfma_f32_16x16x32_bf16 v[120:123], v[152:155], v[172:175], v[120:123]
	s_waitcnt lgkmcnt(5)
	v_mfma_f32_16x16x32_bf16 v[116:119], v[164:167], v[176:179], v[116:119]
	s_waitcnt lgkmcnt(4)
	v_mfma_f32_16x16x32_bf16 v[116:119], v[160:163], v[180:183], v[116:119]
	v_mfma_f32_16x16x32_bf16 v[112:115], v[156:159], v[176:179], v[112:115]
	s_nop 0
	v_mfma_f32_16x16x32_bf16 v[112:115], v[152:155], v[180:183], v[112:115]
	s_waitcnt lgkmcnt(3)
	v_mfma_f32_16x16x32_bf16 v[108:111], v[164:167], v[184:187], v[108:111]
	s_waitcnt lgkmcnt(2)
	v_mfma_f32_16x16x32_bf16 v[108:111], v[160:163], v[188:191], v[108:111]
	v_mfma_f32_16x16x32_bf16 v[104:107], v[156:159], v[184:187], v[104:107]
	s_nop 0
	v_mfma_f32_16x16x32_bf16 v[104:107], v[152:155], v[188:191], v[104:107]
	s_waitcnt lgkmcnt(1)
	v_mfma_f32_16x16x32_bf16 v[100:103], v[164:167], v[192:195], v[100:103]
	s_waitcnt lgkmcnt(0)
	v_mfma_f32_16x16x32_bf16 v[100:103], v[160:163], v[196:199], v[100:103]
	v_mfma_f32_16x16x32_bf16 v[96:99], v[156:159], v[192:195], v[96:99]
	s_nop 0
	v_mfma_f32_16x16x32_bf16 v[96:99], v[152:155], v[196:199], v[96:99]
	s_setprio 0
	s_setprio 1
	v_mfma_f32_16x16x32_bf16 v[92:95], v[148:151], v[168:171], v[92:95]
	s_nop 0
	v_mfma_f32_16x16x32_bf16 v[92:95], v[144:147], v[172:175], v[92:95]
	v_mfma_f32_16x16x32_bf16 v[88:91], v[140:143], v[168:171], v[88:91]
	s_nop 0
	v_mfma_f32_16x16x32_bf16 v[88:91], v[136:139], v[172:175], v[88:91]
	v_mfma_f32_16x16x32_bf16 v[84:87], v[148:151], v[176:179], v[84:87]
	s_nop 0
	v_mfma_f32_16x16x32_bf16 v[84:87], v[144:147], v[180:183], v[84:87]
	v_mfma_f32_16x16x32_bf16 v[80:83], v[140:143], v[176:179], v[80:83]
	s_nop 0
	v_mfma_f32_16x16x32_bf16 v[80:83], v[136:139], v[180:183], v[80:83]
	v_mfma_f32_16x16x32_bf16 v[76:79], v[148:151], v[184:187], v[76:79]
	s_nop 0
	v_mfma_f32_16x16x32_bf16 v[76:79], v[144:147], v[188:191], v[76:79]
	v_mfma_f32_16x16x32_bf16 v[72:75], v[140:143], v[184:187], v[72:75]
	s_nop 0
	v_mfma_f32_16x16x32_bf16 v[72:75], v[136:139], v[188:191], v[72:75]
	v_mfma_f32_16x16x32_bf16 v[68:71], v[148:151], v[192:195], v[68:71]
	s_nop 0
	v_mfma_f32_16x16x32_bf16 v[68:71], v[144:147], v[196:199], v[68:71]
	v_mfma_f32_16x16x32_bf16 v[64:67], v[140:143], v[192:195], v[64:67]
	s_nop 0
	v_mfma_f32_16x16x32_bf16 v[64:67], v[136:139], v[196:199], v[64:67]
	s_setprio 0
	s_barrier
	ds_read_b128 v[168:171], v233 offset:49152
	ds_read_b128 v[172:175], v233 offset:50176
	ds_read_b128 v[176:179], v233 offset:51200
	ds_read_b128 v[180:183], v233 offset:52224
	ds_read_b128 v[184:187], v233 offset:53248
	ds_read_b128 v[188:191], v233 offset:54272
	ds_read_b128 v[192:195], v233 offset:55296
	ds_read_b128 v[196:199], v233 offset:56320
	s_mov_b32 m0, s76
	s_mov_b32 s14, s10
	s_mov_b32 s15, s11
	buffer_load_dwordx4 v215, s[12:15], s5 offen lds
	s_add_i32 s5, s36, 0x100180
	s_mov_b32 m0, s77
	s_nop 0
	buffer_load_dwordx4 v215, s[12:15], s5 offen lds
	s_add_i32 s5, s36, 0x10180
	s_mov_b32 m0, s80
	s_nop 0
	buffer_load_dwordx4 v215, s[12:15], s5 offen lds
	s_add_i32 s5, s36, 0x110180
	s_mov_b32 m0, s81
	s_nop 0
	buffer_load_dwordx4 v215, s[12:15], s5 offen lds
	s_mov_b32 m0, s78
	s_nop 0
	buffer_load_dwordx4 v214, s[8:11], s4 offen lds
	s_add_i32 s4, s60, 0x80180
	s_mov_b32 m0, s79
	s_nop 0
	buffer_load_dwordx4 v214, s[8:11], s4 offen lds
	s_waitcnt vmcnt(8)
	s_waitcnt lgkmcnt(0)
	s_barrier
	s_setprio 1
	s_waitcnt lgkmcnt(7)
	v_mfma_f32_16x16x32_bf16 v[60:63], v[164:167], v[168:171], v[60:63]
	s_waitcnt lgkmcnt(6)
	v_mfma_f32_16x16x32_bf16 v[60:63], v[160:163], v[172:175], v[60:63]
	v_mfma_f32_16x16x32_bf16 v[56:59], v[156:159], v[168:171], v[56:59]
	s_nop 0
	v_mfma_f32_16x16x32_bf16 v[56:59], v[152:155], v[172:175], v[56:59]
	s_waitcnt lgkmcnt(5)
	v_mfma_f32_16x16x32_bf16 v[52:55], v[164:167], v[176:179], v[52:55]
	s_waitcnt lgkmcnt(4)
	v_mfma_f32_16x16x32_bf16 v[52:55], v[160:163], v[180:183], v[52:55]
	v_mfma_f32_16x16x32_bf16 v[48:51], v[156:159], v[176:179], v[48:51]
	s_nop 0
	v_mfma_f32_16x16x32_bf16 v[48:51], v[152:155], v[180:183], v[48:51]
	s_waitcnt lgkmcnt(3)
	v_mfma_f32_16x16x32_bf16 v[44:47], v[164:167], v[184:187], v[44:47]
	s_waitcnt lgkmcnt(2)
	v_mfma_f32_16x16x32_bf16 v[44:47], v[160:163], v[188:191], v[44:47]
	v_mfma_f32_16x16x32_bf16 v[40:43], v[156:159], v[184:187], v[40:43]
	s_nop 0
	v_mfma_f32_16x16x32_bf16 v[40:43], v[152:155], v[188:191], v[40:43]
	s_waitcnt lgkmcnt(1)
	v_mfma_f32_16x16x32_bf16 v[36:39], v[164:167], v[192:195], v[36:39]
	s_waitcnt lgkmcnt(0)
	v_mfma_f32_16x16x32_bf16 v[36:39], v[160:163], v[196:199], v[36:39]
	v_mfma_f32_16x16x32_bf16 v[32:35], v[156:159], v[192:195], v[32:35]
	s_nop 0
	v_mfma_f32_16x16x32_bf16 v[32:35], v[152:155], v[196:199], v[32:35]
	s_setprio 0
	s_setprio 1
	v_mfma_f32_16x16x32_bf16 v[28:31], v[148:151], v[168:171], v[28:31]
	s_nop 0
	v_mfma_f32_16x16x32_bf16 v[28:31], v[144:147], v[172:175], v[28:31]
	v_mfma_f32_16x16x32_bf16 v[24:27], v[140:143], v[168:171], v[24:27]
	s_nop 0
	v_mfma_f32_16x16x32_bf16 v[24:27], v[136:139], v[172:175], v[24:27]
	v_mfma_f32_16x16x32_bf16 v[20:23], v[148:151], v[176:179], v[20:23]
	s_nop 0
	v_mfma_f32_16x16x32_bf16 v[20:23], v[144:147], v[180:183], v[20:23]
	v_mfma_f32_16x16x32_bf16 v[16:19], v[140:143], v[176:179], v[16:19]
	s_nop 0
	v_mfma_f32_16x16x32_bf16 v[16:19], v[136:139], v[180:183], v[16:19]
	v_mfma_f32_16x16x32_bf16 v[12:15], v[148:151], v[184:187], v[12:15]
	s_nop 0
	v_mfma_f32_16x16x32_bf16 v[12:15], v[144:147], v[188:191], v[12:15]
	v_mfma_f32_16x16x32_bf16 v[8:11], v[140:143], v[184:187], v[8:11]
	s_nop 0
	v_mfma_f32_16x16x32_bf16 v[8:11], v[136:139], v[188:191], v[8:11]
	v_mfma_f32_16x16x32_bf16 v[4:7], v[148:151], v[192:195], v[4:7]
	s_nop 0
	v_mfma_f32_16x16x32_bf16 v[4:7], v[144:147], v[196:199], v[4:7]
	v_mfma_f32_16x16x32_bf16 v[0:3], v[140:143], v[192:195], v[0:3]
	s_nop 0
	v_mfma_f32_16x16x32_bf16 v[0:3], v[136:139], v[196:199], v[0:3]
	s_setprio 0
	s_barrier
	s_waitcnt vmcnt(14)
	v_mul_f32_e32 v132, 0x42800000, v132
	v_mul_f32_e32 v128, 0x42800000, v128
	v_mul_f32_e32 v133, 0x42800000, v133
	v_mul_f32_e32 v129, 0x42800000, v129
	v_mul_f32_e32 v134, 0x42800000, v134
	v_mul_f32_e32 v130, 0x42800000, v130
	v_mul_f32_e32 v135, 0x42800000, v135
	v_mul_f32_e32 v131, 0x42800000, v131
	v_cvt_pk_fp8_f32 v204, v128, v132
	v_cvt_pk_fp8_f32 v234, v129, v133
	v_cvt_pk_fp8_f32 v235, v130, v134
	v_cvt_pk_fp8_f32 v236, v131, v135
	s_add_i32 s33, s36, 0x200
	s_mov_b32 s61, 0
	s_mov_b32 s66, s75
	s_mov_b32 s94, s86
	s_branch .LBB0_347

.Lp2_top:
	ds_read_b128 v[158:161], v217
	ds_read_b128 v[162:165], v218
	ds_read_b128 v[166:169], v219
	ds_read_b128 v[170:173], v220
	ds_read_b128 v[148:151], v221
	ds_read_b128 v[144:147], v222
	ds_read_b128 v[140:143], v223
	ds_read_b128 v[136:139], v224
	ds_read_b128 v[174:177], v233
	ds_read_b128 v[178:181], v233 offset:1024
	ds_read_b128 v[182:185], v233 offset:2048
	ds_read_b128 v[186:189], v233 offset:3072
	ds_read_b128 v[190:193], v233 offset:4096
	ds_read_b128 v[194:197], v233 offset:5120
	ds_read_b128 v[234:237], v233 offset:6144
	ds_read_b128 v[238:241], v233 offset:7168
	s_add_i32 s4, s60, s61
	s_mov_b32 s46, s94
	s_add_i32 s94, s94, 1
	s_add_i32 s5, s4, 0x200
	s_add_i32 s16, s33, s61
	s_cmpk_eq_i32 s61, 0x1e00
	s_cselect_b32 s47, s90, s5
	s_cselect_b32 s97, s91, s16
	s_add_i32 s96, s47, 0x80
	s_mov_b32 m0, s82
	s_add_i32 s5, s4, 0x100180
	buffer_load_dwordx4 v214, s[8:11], s5 offen lds
	s_add_i32 s4, s4, 0x180180
	s_mov_b32 m0, s85
	s_add_i32 vcc_lo, s97, 0x80
	buffer_load_dwordx4 v214, s[8:11], s4 offen lds
	s_lshr_b32 s4, s94, 2
	s_mul_i32 s5, s4, s34
	s_add_i32 s16, s5, s2
	s_cmp_lt_i32 s4, s3
	s_cselect_b64 s[4:5], -1, 0
	s_and_b64 s[44:45], s[4:5], exec
	s_cselect_b32 s16, s16, 0
	s_bfe_u32 s17, s94, 0x10001
	s_or_b32 s17, s17, s83
	s_bfe_u32 s67, s16, 0x50007
	s_bfe_u32 s36, s16, 0x50002
	s_and_b32 s95, s16, 3
	s_cmpk_gt_i32 s16, 0xfff
	s_cselect_b64 s[44:45], -1, 0
	v_lshl_or_b32 v156, s17, 3, v216
	s_and_b64 s[16:17], s[44:45], exec
	s_cselect_b32 s16, s25, s21
	s_cselect_b32 s17, s24, s20
	s_lshl_b32 vcc_hi, s67, 23
	s_add_u32 s17, s17, vcc_hi
	s_addc_u32 s16, s16, 0
	s_lshl_b32 vcc_hi, s36, 18
	s_add_u32 s17, s17, vcc_hi
	s_addc_u32 vcc_hi, s16, 0
	s_lshl_b32 s16, s95, 9
	s_add_u32 s16, s17, s16
	v_and_or_b32 v204, s66, 2, v200
	s_addc_u32 s17, vcc_hi, 0
	v_lshlrev_b64 v[128:129], 11, v[204:205]
	v_lshl_add_u64 v[128:129], s[16:17], 0, v[128:129]
	v_lshlrev_b32_e32 v204, 4, v156
	v_lshl_add_u64 v[132:133], v[128:129], 0, v[204:205]
	global_load_dwordx4 v[128:131], v[132:133], off nt
	s_nop 0
	global_load_dwordx4 v[132:135], v[132:133], off offset:2048 nt
	s_waitcnt vmcnt(10)
	s_waitcnt lgkmcnt(8)
	s_barrier
	s_setprio 1
	s_waitcnt lgkmcnt(7)
	v_mfma_f32_16x16x32_bf16 v[124:127], v[158:161], v[174:177], v[124:127]
	s_waitcnt lgkmcnt(6)
	v_mfma_f32_16x16x32_bf16 v[124:127], v[162:165], v[178:181], v[124:127]
	v_mfma_f32_16x16x32_bf16 v[120:123], v[166:169], v[174:177], v[120:123]
	s_nop 0
	v_mfma_f32_16x16x32_bf16 v[120:123], v[170:173], v[178:181], v[120:123]
	s_waitcnt lgkmcnt(5)
	v_mfma_f32_16x16x32_bf16 v[116:119], v[158:161], v[182:185], v[116:119]
	s_waitcnt lgkmcnt(4)
	v_mfma_f32_16x16x32_bf16 v[116:119], v[162:165], v[186:189], v[116:119]
	v_mfma_f32_16x16x32_bf16 v[112:115], v[166:169], v[182:185], v[112:115]
	s_nop 0
	v_mfma_f32_16x16x32_bf16 v[112:115], v[170:173], v[186:189], v[112:115]
	s_waitcnt lgkmcnt(3)
	v_mfma_f32_16x16x32_bf16 v[108:111], v[158:161], v[190:193], v[108:111]
	s_waitcnt lgkmcnt(2)
	v_mfma_f32_16x16x32_bf16 v[108:111], v[162:165], v[194:197], v[108:111]
	v_mfma_f32_16x16x32_bf16 v[104:107], v[166:169], v[190:193], v[104:107]
	s_nop 0
	v_mfma_f32_16x16x32_bf16 v[104:107], v[170:173], v[194:197], v[104:107]
	s_waitcnt lgkmcnt(1)
	v_mfma_f32_16x16x32_bf16 v[100:103], v[158:161], v[234:237], v[100:103]
	s_waitcnt lgkmcnt(0)
	v_mfma_f32_16x16x32_bf16 v[100:103], v[162:165], v[238:241], v[100:103]
	v_mfma_f32_16x16x32_bf16 v[96:99], v[166:169], v[234:237], v[96:99]
	s_nop 0
	v_mfma_f32_16x16x32_bf16 v[96:99], v[170:173], v[238:241], v[96:99]
	s_setprio 0
	s_setprio 1
	v_mfma_f32_16x16x32_bf16 v[92:95], v[148:151], v[174:177], v[92:95]
	s_nop 0
	v_mfma_f32_16x16x32_bf16 v[92:95], v[144:147], v[178:181], v[92:95]
	v_mfma_f32_16x16x32_bf16 v[88:91], v[140:143], v[174:177], v[88:91]
	s_nop 0
	v_mfma_f32_16x16x32_bf16 v[88:91], v[136:139], v[178:181], v[88:91]
	v_mfma_f32_16x16x32_bf16 v[84:87], v[148:151], v[182:185], v[84:87]
	s_nop 0
	v_mfma_f32_16x16x32_bf16 v[84:87], v[144:147], v[186:189], v[84:87]
	v_mfma_f32_16x16x32_bf16 v[80:83], v[140:143], v[182:185], v[80:83]
	s_nop 0
	v_mfma_f32_16x16x32_bf16 v[80:83], v[136:139], v[186:189], v[80:83]
	v_mfma_f32_16x16x32_bf16 v[76:79], v[148:151], v[190:193], v[76:79]
	s_nop 0
	v_mfma_f32_16x16x32_bf16 v[76:79], v[144:147], v[194:197], v[76:79]
	v_mfma_f32_16x16x32_bf16 v[72:75], v[140:143], v[190:193], v[72:75]
	s_nop 0
	v_mfma_f32_16x16x32_bf16 v[72:75], v[136:139], v[194:197], v[72:75]
	v_mfma_f32_16x16x32_bf16 v[68:71], v[148:151], v[234:237], v[68:71]
	s_nop 0
	v_mfma_f32_16x16x32_bf16 v[68:71], v[144:147], v[238:241], v[68:71]
	v_mfma_f32_16x16x32_bf16 v[64:67], v[140:143], v[234:237], v[64:67]
	s_nop 0
	v_mfma_f32_16x16x32_bf16 v[64:67], v[136:139], v[238:241], v[64:67]
	s_setprio 0
	s_barrier
	ds_read_b128 v[174:177], v233 offset:16384
	ds_read_b128 v[178:181], v233 offset:17408
	ds_read_b128 v[182:185], v233 offset:18432
	ds_read_b128 v[186:189], v233 offset:19456
	ds_read_b128 v[190:193], v233 offset:20480
	ds_read_b128 v[194:197], v233 offset:21504
	ds_read_b128 v[234:237], v233 offset:22528
	ds_read_b128 v[238:241], v233 offset:23552
	s_mov_b32 m0, s65
	s_add_i32 s16, s97, 0x100000
	buffer_load_dwordx4 v215, s[12:15], s97 offen lds
	s_mov_b32 m0, s68
	s_nop 0
	buffer_load_dwordx4 v215, s[12:15], s16 offen lds
	s_add_i32 s16, s97, 0x10000
	s_mov_b32 m0, s69
	s_nop 0
	buffer_load_dwordx4 v215, s[12:15], s16 offen lds
	s_add_i32 s16, s97, 0x110000
	s_mov_b32 m0, s70
	s_nop 0
	buffer_load_dwordx4 v215, s[12:15], s16 offen lds
	s_mov_b32 m0, s64
	s_add_i32 s16, s47, 0x80000
	buffer_load_dwordx4 v214, s[8:11], s47 offen lds
	s_mov_b32 m0, s71
	s_nop 0
	buffer_load_dwordx4 v214, s[8:11], s16 offen lds
	s_waitcnt vmcnt(10)
	s_waitcnt lgkmcnt(0)
	s_barrier
	s_setprio 1
	s_waitcnt lgkmcnt(7)
	v_mfma_f32_16x16x32_bf16 v[60:63], v[158:161], v[174:177], v[60:63]
	s_waitcnt lgkmcnt(6)
	v_mfma_f32_16x16x32_bf16 v[60:63], v[162:165], v[178:181], v[60:63]
	v_mfma_f32_16x16x32_bf16 v[56:59], v[166:169], v[174:177], v[56:59]
	s_nop 0
	v_mfma_f32_16x16x32_bf16 v[56:59], v[170:173], v[178:181], v[56:59]
	s_waitcnt lgkmcnt(5)
	v_mfma_f32_16x16x32_bf16 v[52:55], v[158:161], v[182:185], v[52:55]
	s_waitcnt lgkmcnt(4)
	v_mfma_f32_16x16x32_bf16 v[52:55], v[162:165], v[186:189], v[52:55]
	v_mfma_f32_16x16x32_bf16 v[48:51], v[166:169], v[182:185], v[48:51]
	s_nop 0
	v_mfma_f32_16x16x32_bf16 v[48:51], v[170:173], v[186:189], v[48:51]
	s_waitcnt lgkmcnt(3)
	v_mfma_f32_16x16x32_bf16 v[44:47], v[158:161], v[190:193], v[44:47]
	s_waitcnt lgkmcnt(2)
	v_mfma_f32_16x16x32_bf16 v[44:47], v[162:165], v[194:197], v[44:47]
	v_mfma_f32_16x16x32_bf16 v[40:43], v[166:169], v[190:193], v[40:43]
	s_nop 0
	v_mfma_f32_16x16x32_bf16 v[40:43], v[170:173], v[194:197], v[40:43]
	s_waitcnt lgkmcnt(1)
	v_mfma_f32_16x16x32_bf16 v[36:39], v[158:161], v[234:237], v[36:39]
	s_waitcnt lgkmcnt(0)
	v_mfma_f32_16x16x32_bf16 v[36:39], v[162:165], v[238:241], v[36:39]
	v_mfma_f32_16x16x32_bf16 v[32:35], v[166:169], v[234:237], v[32:35]
	s_nop 0
	v_mfma_f32_16x16x32_bf16 v[32:35], v[170:173], v[238:241], v[32:35]
	s_setprio 0
	s_setprio 1
	v_mfma_f32_16x16x32_bf16 v[28:31], v[148:151], v[174:177], v[28:31]
	s_nop 0
	v_mfma_f32_16x16x32_bf16 v[28:31], v[144:147], v[178:181], v[28:31]
	v_mfma_f32_16x16x32_bf16 v[24:27], v[140:143], v[174:177], v[24:27]
	s_nop 0
	v_mfma_f32_16x16x32_bf16 v[24:27], v[136:139], v[178:181], v[24:27]
	v_mfma_f32_16x16x32_bf16 v[20:23], v[148:151], v[182:185], v[20:23]
	s_nop 0
	v_mfma_f32_16x16x32_bf16 v[20:23], v[144:147], v[186:189], v[20:23]
	v_mfma_f32_16x16x32_bf16 v[16:19], v[140:143], v[182:185], v[16:19]
	s_nop 0
	v_mfma_f32_16x16x32_bf16 v[16:19], v[136:139], v[186:189], v[16:19]
	v_mfma_f32_16x16x32_bf16 v[12:15], v[148:151], v[190:193], v[12:15]
	s_nop 0
	v_mfma_f32_16x16x32_bf16 v[12:15], v[144:147], v[194:197], v[12:15]
	v_mfma_f32_16x16x32_bf16 v[8:11], v[140:143], v[190:193], v[8:11]
	s_nop 0
	v_mfma_f32_16x16x32_bf16 v[8:11], v[136:139], v[194:197], v[8:11]
	v_mfma_f32_16x16x32_bf16 v[4:7], v[148:151], v[234:237], v[4:7]
	s_nop 0
	v_mfma_f32_16x16x32_bf16 v[4:7], v[144:147], v[238:241], v[4:7]
	v_mfma_f32_16x16x32_bf16 v[0:3], v[140:143], v[234:237], v[0:3]
	s_nop 0
	v_mfma_f32_16x16x32_bf16 v[0:3], v[136:139], v[238:241], v[0:3]
	s_setprio 0
	s_barrier
	ds_read_b128 v[136:139], v225
	ds_read_b128 v[140:143], v226
	ds_read_b128 v[144:147], v227
	ds_read_b128 v[148:151], v228
	ds_read_b128 v[158:161], v229
	ds_read_b128 v[162:165], v230
	ds_read_b128 v[166:169], v231
	ds_read_b128 v[170:173], v232
	ds_read_b128 v[174:177], v233 offset:32768
	ds_read_b128 v[178:181], v233 offset:33792
	ds_read_b128 v[182:185], v233 offset:34816
	ds_read_b128 v[186:189], v233 offset:35840
	ds_read_b128 v[190:193], v233 offset:36864
	ds_read_b128 v[194:197], v233 offset:37888
	ds_read_b128 v[234:237], v233 offset:38912
	ds_read_b128 v[238:241], v233 offset:39936
	s_mov_b32 m0, s72
	s_add_i32 s16, s47, 0x100000
	buffer_load_dwordx4 v214, s[8:11], s16 offen lds
	s_add_i32 s16, s47, 0x180000
	s_mov_b32 m0, s73
	s_nop 0
	buffer_load_dwordx4 v214, s[8:11], s16 offen lds
	s_waitcnt vmcnt(10)
	s_waitcnt lgkmcnt(8)
	s_barrier
	s_setprio 1
	s_waitcnt lgkmcnt(7)
	v_mfma_f32_16x16x32_bf16 v[124:127], v[136:139], v[174:177], v[124:127]
	s_waitcnt lgkmcnt(6)
	v_mfma_f32_16x16x32_bf16 v[124:127], v[140:143], v[178:181], v[124:127]
	v_mfma_f32_16x16x32_bf16 v[120:123], v[144:147], v[174:177], v[120:123]
	s_nop 0
	v_mfma_f32_16x16x32_bf16 v[120:123], v[148:151], v[178:181], v[120:123]
	s_waitcnt lgkmcnt(5)
	v_mfma_f32_16x16x32_bf16 v[116:119], v[136:139], v[182:185], v[116:119]
	s_waitcnt lgkmcnt(4)
	v_mfma_f32_16x16x32_bf16 v[116:119], v[140:143], v[186:189], v[116:119]
	v_mfma_f32_16x16x32_bf16 v[112:115], v[144:147], v[182:185], v[112:115]
	s_nop 0
	v_mfma_f32_16x16x32_bf16 v[112:115], v[148:151], v[186:189], v[112:115]
	s_waitcnt lgkmcnt(3)
	v_mfma_f32_16x16x32_bf16 v[108:111], v[136:139], v[190:193], v[108:111]
	s_waitcnt lgkmcnt(2)
	v_mfma_f32_16x16x32_bf16 v[108:111], v[140:143], v[194:197], v[108:111]
	v_mfma_f32_16x16x32_bf16 v[104:107], v[144:147], v[190:193], v[104:107]
	s_nop 0
	v_mfma_f32_16x16x32_bf16 v[104:107], v[148:151], v[194:197], v[104:107]
	s_waitcnt lgkmcnt(1)
	v_mfma_f32_16x16x32_bf16 v[100:103], v[136:139], v[234:237], v[100:103]
	s_waitcnt lgkmcnt(0)
	v_mfma_f32_16x16x32_bf16 v[100:103], v[140:143], v[238:241], v[100:103]
	v_mfma_f32_16x16x32_bf16 v[96:99], v[144:147], v[234:237], v[96:99]
	s_nop 0
	v_mfma_f32_16x16x32_bf16 v[96:99], v[148:151], v[238:241], v[96:99]
	s_setprio 0
	s_setprio 1
	v_mfma_f32_16x16x32_bf16 v[92:95], v[158:161], v[174:177], v[92:95]
	s_nop 0
	v_mfma_f32_16x16x32_bf16 v[92:95], v[162:165], v[178:181], v[92:95]
	v_mfma_f32_16x16x32_bf16 v[88:91], v[166:169], v[174:177], v[88:91]
	s_nop 0
	v_mfma_f32_16x16x32_bf16 v[88:91], v[170:173], v[178:181], v[88:91]
	v_mfma_f32_16x16x32_bf16 v[84:87], v[158:161], v[182:185], v[84:87]
	s_nop 0
	v_mfma_f32_16x16x32_bf16 v[84:87], v[162:165], v[186:189], v[84:87]
	v_mfma_f32_16x16x32_bf16 v[80:83], v[166:169], v[182:185], v[80:83]
	s_nop 0
	v_mfma_f32_16x16x32_bf16 v[80:83], v[170:173], v[186:189], v[80:83]
	v_mfma_f32_16x16x32_bf16 v[76:79], v[158:161], v[190:193], v[76:79]
	s_nop 0
	v_mfma_f32_16x16x32_bf16 v[76:79], v[162:165], v[194:197], v[76:79]
	v_mfma_f32_16x16x32_bf16 v[72:75], v[166:169], v[190:193], v[72:75]
	s_nop 0
	v_mfma_f32_16x16x32_bf16 v[72:75], v[170:173], v[194:197], v[72:75]
	v_mfma_f32_16x16x32_bf16 v[68:71], v[158:161], v[234:237], v[68:71]
	s_nop 0
	v_mfma_f32_16x16x32_bf16 v[68:71], v[162:165], v[238:241], v[68:71]
	v_mfma_f32_16x16x32_bf16 v[64:67], v[166:169], v[234:237], v[64:67]
	s_nop 0
	v_mfma_f32_16x16x32_bf16 v[64:67], v[170:173], v[238:241], v[64:67]
	s_setprio 0
	s_barrier
	ds_read_b128 v[174:177], v233 offset:49152
	ds_read_b128 v[178:181], v233 offset:50176
	ds_read_b128 v[182:185], v233 offset:51200
	ds_read_b128 v[186:189], v233 offset:52224
	ds_read_b128 v[190:193], v233 offset:53248
	ds_read_b128 v[194:197], v233 offset:54272
	ds_read_b128 v[234:237], v233 offset:55296
	ds_read_b128 v[238:241], v233 offset:56320
	s_mov_b32 m0, s76
	s_add_i32 s16, s97, 0x100080
	buffer_load_dwordx4 v215, s[12:15], vcc_lo offen lds
	s_mov_b32 m0, s77
	s_add_i32 s47, s47, 0x80080
	buffer_load_dwordx4 v215, s[12:15], s16 offen lds
	s_add_i32 s16, s97, 0x10080
	s_mov_b32 m0, s80
	s_add_i32 s97, s97, 0x110080
	buffer_load_dwordx4 v215, s[12:15], s16 offen lds
	s_mov_b32 m0, s81
	s_nop 0
	buffer_load_dwordx4 v215, s[12:15], s97 offen lds
	s_mov_b32 m0, s78
	s_nop 0
	buffer_load_dwordx4 v214, s[8:11], s96 offen lds
	s_mov_b32 m0, s79
	s_nop 0
	buffer_load_dwordx4 v214, s[8:11], s47 offen lds
	s_bitcmp0_b32 s46, 0
	s_mov_b32 s98, 0xffff
	s_cselect_b32 s98, 0xffff0000, s98
	s_waitcnt vmcnt(8)
	s_waitcnt lgkmcnt(0)
	s_barrier
	s_setprio 1
	s_waitcnt lgkmcnt(7)
	v_mfma_f32_16x16x32_bf16 v[60:63], v[136:139], v[174:177], v[60:63]
	s_waitcnt lgkmcnt(6)
	v_mfma_f32_16x16x32_bf16 v[60:63], v[140:143], v[178:181], v[60:63]
	v_mfma_f32_16x16x32_bf16 v[56:59], v[144:147], v[174:177], v[56:59]
	v_mul_f32_e32 v128, 0x42800000, v128
	v_mfma_f32_16x16x32_bf16 v[56:59], v[148:151], v[178:181], v[56:59]
	v_mul_f32_e32 v130, 0x42800000, v130
	s_waitcnt lgkmcnt(5)
	v_mfma_f32_16x16x32_bf16 v[52:55], v[136:139], v[182:185], v[52:55]
	s_waitcnt lgkmcnt(4)
	v_mfma_f32_16x16x32_bf16 v[52:55], v[140:143], v[186:189], v[52:55]
	v_mfma_f32_16x16x32_bf16 v[48:51], v[144:147], v[182:185], v[48:51]
	v_mul_f32_e32 v132, 0x42800000, v132
	v_mfma_f32_16x16x32_bf16 v[48:51], v[148:151], v[186:189], v[48:51]
	v_mul_f32_e32 v134, 0x42800000, v134
	s_waitcnt lgkmcnt(3)
	v_mfma_f32_16x16x32_bf16 v[44:47], v[136:139], v[190:193], v[44:47]
	s_waitcnt lgkmcnt(2)
	v_mfma_f32_16x16x32_bf16 v[44:47], v[140:143], v[194:197], v[44:47]
	v_mfma_f32_16x16x32_bf16 v[40:43], v[144:147], v[190:193], v[40:43]
	v_mul_f32_e32 v129, 0x42800000, v129
	v_mfma_f32_16x16x32_bf16 v[40:43], v[148:151], v[194:197], v[40:43]
	v_mul_f32_e32 v131, 0x42800000, v131
	s_waitcnt lgkmcnt(1)
	v_mfma_f32_16x16x32_bf16 v[36:39], v[136:139], v[234:237], v[36:39]
	s_waitcnt lgkmcnt(0)
	v_mfma_f32_16x16x32_bf16 v[36:39], v[140:143], v[238:241], v[36:39]
	v_mfma_f32_16x16x32_bf16 v[32:35], v[144:147], v[234:237], v[32:35]
	v_mul_f32_e32 v133, 0x42800000, v133
	v_mfma_f32_16x16x32_bf16 v[32:35], v[148:151], v[238:241], v[32:35]
	v_mul_f32_e32 v135, 0x42800000, v135
	s_setprio 0
	s_setprio 1
	v_mfma_f32_16x16x32_bf16 v[28:31], v[158:161], v[174:177], v[28:31]
	v_cvt_pk_fp8_f32 v204, v128, v132
	v_mfma_f32_16x16x32_bf16 v[28:31], v[162:165], v[178:181], v[28:31]
	v_mfma_f32_16x16x32_bf16 v[24:27], v[166:169], v[174:177], v[24:27]
	v_cvt_pk_fp8_f32 v204, v128, v132 op_sel:[0,0,1]
	v_mfma_f32_16x16x32_bf16 v[24:27], v[170:173], v[178:181], v[24:27]
	v_mfma_f32_16x16x32_bf16 v[20:23], v[158:161], v[182:185], v[20:23]
	v_cvt_pk_fp8_f32 v250, v129, v133
	v_mfma_f32_16x16x32_bf16 v[20:23], v[162:165], v[186:189], v[20:23]
	v_mfma_f32_16x16x32_bf16 v[16:19], v[166:169], v[182:185], v[16:19]
	v_cvt_pk_fp8_f32 v250, v129, v133 op_sel:[0,0,1]
	v_mfma_f32_16x16x32_bf16 v[16:19], v[170:173], v[186:189], v[16:19]
	v_mfma_f32_16x16x32_bf16 v[12:15], v[158:161], v[190:193], v[12:15]
	v_cvt_pk_fp8_f32 v251, v130, v134
	v_mfma_f32_16x16x32_bf16 v[12:15], v[162:165], v[194:197], v[12:15]
	v_bfi_b32 v152, s98, v204, v152
	v_mfma_f32_16x16x32_bf16 v[8:11], v[166:169], v[190:193], v[8:11]
	v_cvt_pk_fp8_f32 v251, v130, v134 op_sel:[0,0,1]
	v_mfma_f32_16x16x32_bf16 v[8:11], v[170:173], v[194:197], v[8:11]
	v_bfi_b32 v153, s98, v250, v153
	v_mfma_f32_16x16x32_bf16 v[4:7], v[158:161], v[234:237], v[4:7]
	v_cvt_pk_fp8_f32 v252, v131, v135
	v_mfma_f32_16x16x32_bf16 v[4:7], v[162:165], v[238:241], v[4:7]
	v_bfi_b32 v154, s98, v251, v154
	v_mfma_f32_16x16x32_bf16 v[0:3], v[166:169], v[234:237], v[0:3]
	v_cvt_pk_fp8_f32 v252, v131, v135 op_sel:[0,0,1]
	v_mfma_f32_16x16x32_bf16 v[0:3], v[170:173], v[238:241], v[0:3]
	v_bfi_b32 v155, s98, v252, v155
	s_setprio 0
	s_barrier
	s_bitcmp0_b32 s46, 0
	s_mov_b64 s[46:47], -1
	s_cbranch_scc0 .LBB0_345
	s_andn2_b64 vcc, exec, s[4:5]
	s_cbranch_vccnz .LBB0_345
	s_lshl_b32 s4, s67, 10
	s_lshl_b32 s5, s95, 8
	s_or_b32 s16, s4, s5
	s_and_b64 s[4:5], s[44:45], exec
	s_cselect_b32 s4, 8, 0
	v_lshlrev_b32_e32 v128, 3, v156
	s_or_b32 s4, s4, s16
	v_and_b32_e32 v128, 0xf0, v128
	v_or_b32_e32 v128, s4, v128
	v_or_b32_e32 v204, v128, v202
	v_lshlrev_b64 v[128:129], 12, v[204:205]
	v_lshl_add_u64 v[128:129], s[6:7], 0, v[128:129]
	s_lshl_b32 s36, s36, 7
	v_lshl_add_u64 v[128:129], v[128:129], 0, s[36:37]
	v_lshl_add_u64 v[128:129], v[128:129], 0, v[200:201]
	v_add_co_u32_e32 v130, vcc, 0x1000, v128
	global_store_dword v[128:129], v152, off
	s_nop 0
	v_addc_co_u32_e32 v131, vcc, 0, v129, vcc
	global_store_dword v[130:131], v153, off
	v_add_co_u32_e32 v130, vcc, 0x2000, v128
	s_nop 1
	v_addc_co_u32_e32 v131, vcc, 0, v129, vcc
	v_add_co_u32_e32 v128, vcc, 0x3000, v128
	global_store_dword v[130:131], v154, off
	s_nop 0
	v_addc_co_u32_e32 v129, vcc, 0, v129, vcc
	global_store_dword v[128:129], v155, off
	s_branch .LBB0_345

.LBB0_592:
	s_waitcnt lgkmcnt(0)
	s_add_i32 s4, s60, 0x180
	s_add_i32 s5, s42, 0x180
	s_barrier
	s_setprio 1
	s_waitcnt lgkmcnt(7)
	v_mfma_f32_16x16x32_bf16 v[60:63], v[164:167], v[196:199], 0
	s_waitcnt lgkmcnt(6)
	v_mfma_f32_16x16x32_bf16 v[60:63], v[160:163], v[192:195], v[60:63]
	v_mfma_f32_16x16x32_bf16 v[56:59], v[156:159], v[196:199], 0
	s_nop 0
	v_mfma_f32_16x16x32_bf16 v[56:59], v[152:155], v[192:195], v[56:59]
	s_waitcnt lgkmcnt(5)
	v_mfma_f32_16x16x32_bf16 v[52:55], v[164:167], v[188:191], 0
	s_waitcnt lgkmcnt(4)
	v_mfma_f32_16x16x32_bf16 v[52:55], v[160:163], v[184:187], v[52:55]
	v_mfma_f32_16x16x32_bf16 v[48:51], v[156:159], v[188:191], 0
	s_nop 0
	v_mfma_f32_16x16x32_bf16 v[48:51], v[152:155], v[184:187], v[48:51]
	s_waitcnt lgkmcnt(3)
	v_mfma_f32_16x16x32_bf16 v[44:47], v[164:167], v[180:183], 0
	s_waitcnt lgkmcnt(2)
	v_mfma_f32_16x16x32_bf16 v[44:47], v[160:163], v[176:179], v[44:47]
	v_mfma_f32_16x16x32_bf16 v[40:43], v[156:159], v[180:183], 0
	s_nop 0
	v_mfma_f32_16x16x32_bf16 v[40:43], v[152:155], v[176:179], v[40:43]
	s_waitcnt lgkmcnt(1)
	v_mfma_f32_16x16x32_bf16 v[36:39], v[164:167], v[172:175], 0
	s_waitcnt lgkmcnt(0)
	v_mfma_f32_16x16x32_bf16 v[36:39], v[160:163], v[168:171], v[36:39]
	v_mfma_f32_16x16x32_bf16 v[32:35], v[156:159], v[172:175], 0
	s_nop 0
	v_mfma_f32_16x16x32_bf16 v[32:35], v[152:155], v[168:171], v[32:35]
	s_setprio 0
	s_setprio 1
	v_mfma_f32_16x16x32_bf16 v[28:31], v[148:151], v[196:199], 0
	s_nop 0
	v_mfma_f32_16x16x32_bf16 v[28:31], v[144:147], v[192:195], v[28:31]
	v_mfma_f32_16x16x32_bf16 v[24:27], v[140:143], v[196:199], 0
	s_nop 0
	v_mfma_f32_16x16x32_bf16 v[24:27], v[136:139], v[192:195], v[24:27]
	v_mfma_f32_16x16x32_bf16 v[20:23], v[148:151], v[188:191], 0
	s_nop 0
	v_mfma_f32_16x16x32_bf16 v[20:23], v[144:147], v[184:187], v[20:23]
	v_mfma_f32_16x16x32_bf16 v[16:19], v[140:143], v[188:191], 0
	s_nop 0
	v_mfma_f32_16x16x32_bf16 v[16:19], v[136:139], v[184:187], v[16:19]
	v_mfma_f32_16x16x32_bf16 v[12:15], v[148:151], v[180:183], 0
	s_nop 0
	v_mfma_f32_16x16x32_bf16 v[12:15], v[144:147], v[176:179], v[12:15]
	v_mfma_f32_16x16x32_bf16 v[8:11], v[140:143], v[180:183], 0
	s_nop 0
	v_mfma_f32_16x16x32_bf16 v[8:11], v[136:139], v[176:179], v[8:11]
	v_mfma_f32_16x16x32_bf16 v[4:7], v[148:151], v[172:175], 0
	s_nop 0
	v_mfma_f32_16x16x32_bf16 v[4:7], v[144:147], v[168:171], v[4:7]
	v_mfma_f32_16x16x32_bf16 v[0:3], v[140:143], v[172:175], 0
	s_nop 0
	v_mfma_f32_16x16x32_bf16 v[0:3], v[136:139], v[168:171], v[0:3]
	s_setprio 0
	s_barrier
	ds_read_b128 v[164:167], v224
	ds_read_b128 v[160:163], v225
	ds_read_b128 v[156:159], v226
	ds_read_b128 v[152:155], v227
	ds_read_b128 v[148:151], v228
	ds_read_b128 v[144:147], v229
	ds_read_b128 v[140:143], v230
	ds_read_b128 v[136:139], v231
	ds_read_b128 v[168:171], v232 offset:32768
	ds_read_b128 v[172:175], v232 offset:33792
	ds_read_b128 v[176:179], v232 offset:34816
	ds_read_b128 v[180:183], v232 offset:35840
	ds_read_b128 v[184:187], v232 offset:36864
	ds_read_b128 v[188:191], v232 offset:37888
	ds_read_b128 v[192:195], v232 offset:38912
	ds_read_b128 v[196:199], v232 offset:39936
	s_mov_b32 m0, s68
	s_add_i32 s10, s60, 0x100100
	buffer_load_dwordx4 v213, s[12:15], s10 offen lds
	s_add_i32 s10, s60, 0x180100
	s_mov_b32 m0, s69
	s_nop 0
	buffer_load_dwordx4 v213, s[12:15], s10 offen lds
	s_waitcnt vmcnt(10)
	s_waitcnt lgkmcnt(8)
	s_barrier
	s_setprio 1
	s_waitcnt lgkmcnt(7)
	v_mfma_f32_16x16x32_bf16 v[124:127], v[164:167], v[168:171], v[124:127]
	s_waitcnt lgkmcnt(6)
	v_mfma_f32_16x16x32_bf16 v[124:127], v[160:163], v[172:175], v[124:127]
	v_mfma_f32_16x16x32_bf16 v[120:123], v[156:159], v[168:171], v[120:123]
	s_nop 0
	v_mfma_f32_16x16x32_bf16 v[120:123], v[152:155], v[172:175], v[120:123]
	s_waitcnt lgkmcnt(5)
	v_mfma_f32_16x16x32_bf16 v[116:119], v[164:167], v[176:179], v[116:119]
	s_waitcnt lgkmcnt(4)
	v_mfma_f32_16x16x32_bf16 v[116:119], v[160:163], v[180:183], v[116:119]
	v_mfma_f32_16x16x32_bf16 v[112:115], v[156:159], v[176:179], v[112:115]
	s_nop 0
	v_mfma_f32_16x16x32_bf16 v[112:115], v[152:155], v[180:183], v[112:115]
	s_waitcnt lgkmcnt(3)
	v_mfma_f32_16x16x32_bf16 v[108:111], v[164:167], v[184:187], v[108:111]
	s_waitcnt lgkmcnt(2)
	v_mfma_f32_16x16x32_bf16 v[108:111], v[160:163], v[188:191], v[108:111]
	v_mfma_f32_16x16x32_bf16 v[104:107], v[156:159], v[184:187], v[104:107]
	s_nop 0
	v_mfma_f32_16x16x32_bf16 v[104:107], v[152:155], v[188:191], v[104:107]
	s_waitcnt lgkmcnt(1)
	v_mfma_f32_16x16x32_bf16 v[100:103], v[164:167], v[192:195], v[100:103]
	s_waitcnt lgkmcnt(0)
	v_mfma_f32_16x16x32_bf16 v[100:103], v[160:163], v[196:199], v[100:103]
	v_mfma_f32_16x16x32_bf16 v[96:99], v[156:159], v[192:195], v[96:99]
	s_nop 0
	v_mfma_f32_16x16x32_bf16 v[96:99], v[152:155], v[196:199], v[96:99]
	s_setprio 0
	s_setprio 1
	v_mfma_f32_16x16x32_bf16 v[92:95], v[148:151], v[168:171], v[92:95]
	s_nop 0
	v_mfma_f32_16x16x32_bf16 v[92:95], v[144:147], v[172:175], v[92:95]
	v_mfma_f32_16x16x32_bf16 v[88:91], v[140:143], v[168:171], v[88:91]
	s_nop 0
	v_mfma_f32_16x16x32_bf16 v[88:91], v[136:139], v[172:175], v[88:91]
	v_mfma_f32_16x16x32_bf16 v[84:87], v[148:151], v[176:179], v[84:87]
	s_nop 0
	v_mfma_f32_16x16x32_bf16 v[84:87], v[144:147], v[180:183], v[84:87]
	v_mfma_f32_16x16x32_bf16 v[80:83], v[140:143], v[176:179], v[80:83]
	s_nop 0
	v_mfma_f32_16x16x32_bf16 v[80:83], v[136:139], v[180:183], v[80:83]
	v_mfma_f32_16x16x32_bf16 v[76:79], v[148:151], v[184:187], v[76:79]
	s_nop 0
	v_mfma_f32_16x16x32_bf16 v[76:79], v[144:147], v[188:191], v[76:79]
	v_mfma_f32_16x16x32_bf16 v[72:75], v[140:143], v[184:187], v[72:75]
	s_nop 0
	v_mfma_f32_16x16x32_bf16 v[72:75], v[136:139], v[188:191], v[72:75]
	v_mfma_f32_16x16x32_bf16 v[68:71], v[148:151], v[192:195], v[68:71]
	s_nop 0
	v_mfma_f32_16x16x32_bf16 v[68:71], v[144:147], v[196:199], v[68:71]
	v_mfma_f32_16x16x32_bf16 v[64:67], v[140:143], v[192:195], v[64:67]
	s_nop 0
	v_mfma_f32_16x16x32_bf16 v[64:67], v[136:139], v[196:199], v[64:67]
	s_setprio 0
	s_barrier
	ds_read_b128 v[168:171], v232 offset:49152
	ds_read_b128 v[172:175], v232 offset:50176
	ds_read_b128 v[176:179], v232 offset:51200
	ds_read_b128 v[180:183], v232 offset:52224
	ds_read_b128 v[184:187], v232 offset:53248
	ds_read_b128 v[188:191], v232 offset:54272
	ds_read_b128 v[192:195], v232 offset:55296
	ds_read_b128 v[196:199], v232 offset:56320
	s_mov_b32 m0, s72
	s_mov_b32 s10, s14
	s_mov_b32 s11, s15
	buffer_load_dwordx4 v214, s[8:11], s5 offen lds
	s_add_i32 s5, s42, 0x40180
	s_mov_b32 m0, s73
	s_nop 0
	buffer_load_dwordx4 v214, s[8:11], s5 offen lds
	s_add_i32 s5, s42, 0x4180
	s_mov_b32 m0, s76
	s_nop 0
	buffer_load_dwordx4 v214, s[8:11], s5 offen lds
	s_add_i32 s5, s42, 0x44180
	s_mov_b32 m0, s77
	s_nop 0
	buffer_load_dwordx4 v214, s[8:11], s5 offen lds
	s_mov_b32 m0, s74
	s_nop 0
	buffer_load_dwordx4 v213, s[12:15], s4 offen lds
	s_add_i32 s4, s60, 0x80180
	s_mov_b32 m0, s75
	s_nop 0
	buffer_load_dwordx4 v213, s[12:15], s4 offen lds
	s_waitcnt vmcnt(8)
	s_waitcnt lgkmcnt(0)
	s_barrier
	s_setprio 1
	s_waitcnt lgkmcnt(7)
	v_mfma_f32_16x16x32_bf16 v[60:63], v[164:167], v[168:171], v[60:63]
	s_waitcnt lgkmcnt(6)
	v_mfma_f32_16x16x32_bf16 v[60:63], v[160:163], v[172:175], v[60:63]
	v_mfma_f32_16x16x32_bf16 v[56:59], v[156:159], v[168:171], v[56:59]
	s_nop 0
	v_mfma_f32_16x16x32_bf16 v[56:59], v[152:155], v[172:175], v[56:59]
	s_waitcnt lgkmcnt(5)
	v_mfma_f32_16x16x32_bf16 v[52:55], v[164:167], v[176:179], v[52:55]
	s_waitcnt lgkmcnt(4)
	v_mfma_f32_16x16x32_bf16 v[52:55], v[160:163], v[180:183], v[52:55]
	v_mfma_f32_16x16x32_bf16 v[48:51], v[156:159], v[176:179], v[48:51]
	s_nop 0
	v_mfma_f32_16x16x32_bf16 v[48:51], v[152:155], v[180:183], v[48:51]
	s_waitcnt lgkmcnt(3)
	v_mfma_f32_16x16x32_bf16 v[44:47], v[164:167], v[184:187], v[44:47]
	s_waitcnt lgkmcnt(2)
	v_mfma_f32_16x16x32_bf16 v[44:47], v[160:163], v[188:191], v[44:47]
	v_mfma_f32_16x16x32_bf16 v[40:43], v[156:159], v[184:187], v[40:43]
	s_nop 0
	v_mfma_f32_16x16x32_bf16 v[40:43], v[152:155], v[188:191], v[40:43]
	s_waitcnt lgkmcnt(1)
	v_mfma_f32_16x16x32_bf16 v[36:39], v[164:167], v[192:195], v[36:39]
	s_waitcnt lgkmcnt(0)
	v_mfma_f32_16x16x32_bf16 v[36:39], v[160:163], v[196:199], v[36:39]
	v_mfma_f32_16x16x32_bf16 v[32:35], v[156:159], v[192:195], v[32:35]
	s_nop 0
	v_mfma_f32_16x16x32_bf16 v[32:35], v[152:155], v[196:199], v[32:35]
	s_setprio 0
	s_setprio 1
	v_mfma_f32_16x16x32_bf16 v[28:31], v[148:151], v[168:171], v[28:31]
	s_nop 0
	v_mfma_f32_16x16x32_bf16 v[28:31], v[144:147], v[172:175], v[28:31]
	v_mfma_f32_16x16x32_bf16 v[24:27], v[140:143], v[168:171], v[24:27]
	s_nop 0
	v_mfma_f32_16x16x32_bf16 v[24:27], v[136:139], v[172:175], v[24:27]
	v_mfma_f32_16x16x32_bf16 v[20:23], v[148:151], v[176:179], v[20:23]
	s_nop 0
	v_mfma_f32_16x16x32_bf16 v[20:23], v[144:147], v[180:183], v[20:23]
	v_mfma_f32_16x16x32_bf16 v[16:19], v[140:143], v[176:179], v[16:19]
	s_nop 0
	v_mfma_f32_16x16x32_bf16 v[16:19], v[136:139], v[180:183], v[16:19]
	v_mfma_f32_16x16x32_bf16 v[12:15], v[148:151], v[184:187], v[12:15]
	s_nop 0
	v_mfma_f32_16x16x32_bf16 v[12:15], v[144:147], v[188:191], v[12:15]
	v_mfma_f32_16x16x32_bf16 v[8:11], v[140:143], v[184:187], v[8:11]
	s_nop 0
	v_mfma_f32_16x16x32_bf16 v[8:11], v[136:139], v[188:191], v[8:11]
	v_mfma_f32_16x16x32_bf16 v[4:7], v[148:151], v[192:195], v[4:7]
	s_nop 0
	v_mfma_f32_16x16x32_bf16 v[4:7], v[144:147], v[196:199], v[4:7]
	v_mfma_f32_16x16x32_bf16 v[0:3], v[140:143], v[192:195], v[0:3]
	s_nop 0
	v_mfma_f32_16x16x32_bf16 v[0:3], v[136:139], v[196:199], v[0:3]
	s_setprio 0
	s_barrier
	s_waitcnt vmcnt(14)
	v_mul_f32_e32 v132, 0x42800000, v132
	v_mul_f32_e32 v128, 0x42800000, v128
	v_mul_f32_e32 v133, 0x42800000, v133
	v_mul_f32_e32 v129, 0x42800000, v129
	v_mul_f32_e32 v134, 0x42800000, v134
	v_mul_f32_e32 v130, 0x42800000, v130
	v_mul_f32_e32 v135, 0x42800000, v135
	v_mul_f32_e32 v131, 0x42800000, v131
	v_cvt_pk_fp8_f32 v202, v128, v132
	v_cvt_pk_fp8_f32 v233, v129, v133
	v_cvt_pk_fp8_f32 v234, v130, v134
	v_cvt_pk_fp8_f32 v235, v131, v135
	s_add_i32 s33, s42, 0x200
	s_mov_b32 s66, 0
	s_mov_b32 s89, s70
	s_mov_b32 s90, s71
	s_branch .LBB0_595

.LBB0_595:
	v_mov_b32_e32 v152, v202
	v_mov_b32_e32 v153, v233
	v_mov_b32_e32 v154, v234
	v_mov_b32_e32 v155, v235
	ds_read_b128 v[158:161], v216
	ds_read_b128 v[162:165], v217
	ds_read_b128 v[166:169], v218
	ds_read_b128 v[170:173], v219
	ds_read_b128 v[148:151], v220
	ds_read_b128 v[144:147], v221
	ds_read_b128 v[140:143], v222
	ds_read_b128 v[136:139], v223
	ds_read_b128 v[174:177], v232
	ds_read_b128 v[178:181], v232 offset:1024
	ds_read_b128 v[182:185], v232 offset:2048
	ds_read_b128 v[186:189], v232 offset:3072
	ds_read_b128 v[190:193], v232 offset:4096
	ds_read_b128 v[194:197], v232 offset:5120
	ds_read_b128 v[234:237], v232 offset:6144
	ds_read_b128 v[238:241], v232 offset:7168
	s_add_i32 s4, s60, s66
	s_mov_b32 s42, s90
	s_add_i32 s90, s90, 1
	s_add_i32 s5, s4, 0x200
	s_add_i32 s67, s33, s66
	s_cmpk_eq_i32 s66, 0x200
	s_cselect_b32 s43, s87, s5
	s_cselect_b32 s93, s88, s67
	s_add_i32 s92, s43, 0x80
	s_mov_b32 m0, s78
	s_add_i32 s5, s4, 0x100180
	buffer_load_dwordx4 v213, s[12:15], s5 offen lds
	s_add_i32 s4, s4, 0x180180
	s_mov_b32 m0, s81
	s_add_i32 s94, s93, 0x80
	buffer_load_dwordx4 v213, s[12:15], s4 offen lds
	s_lshr_b32 s4, s90, 2
	s_mul_i32 s67, s4, s34
	s_add_i32 s67, s67, s2
	s_cmp_lt_i32 s4, s3
	s_cselect_b64 s[4:5], -1, 0
	s_and_b64 s[96:97], s[4:5], exec
	s_cselect_b32 s91, s67, 0
	s_ashr_i32 s96, s91, 7
	s_bfe_u32 s95, s90, 0x10001
	s_ashr_i32 s97, s96, 31
	s_or_b32 s95, s95, s79
	s_lshl_b64 s[96:97], s[96:97], 23
	s_add_u32 s96, s48, s96
	s_addc_u32 s97, s49, s97
	s_lshl_b32 vcc_lo, s91, 16
	s_and_b32 vcc_lo, vcc_lo, 0x600000
	s_add_u32 s96, s96, vcc_lo
	s_addc_u32 s97, s97, 0
	s_lshl_b32 s91, s91, 7
	s_and_b32 s91, s91, 0xf80
	s_lshl_b32 vcc_lo, s91, 2
	s_add_u32 s96, s96, vcc_lo
	v_and_or_b32 v202, s89, 2, v200
	s_addc_u32 s97, s97, 0
	v_lshl_or_b32 v156, s95, 5, v215
	v_lshlrev_b64 v[128:129], 14, v[202:203]
	v_lshl_add_u64 v[128:129], s[96:97], 0, v[128:129]
	v_lshlrev_b32_e32 v202, 2, v156
	v_lshl_add_u64 v[128:129], v[128:129], 0, v[202:203]
	s_movk_i32 s95, 0x4000
	v_add_co_u32_e32 v132, vcc, s95, v128
	s_nop 1
	v_addc_co_u32_e32 v133, vcc, 0, v129, vcc
	global_load_dwordx4 v[128:131], v[128:129], off nt
	s_nop 0
	global_load_dwordx4 v[132:135], v[132:133], off nt
	s_waitcnt vmcnt(10)
	s_waitcnt lgkmcnt(8)
	s_barrier
	s_setprio 1
	s_waitcnt lgkmcnt(7)
	v_mfma_f32_16x16x32_bf16 v[124:127], v[158:161], v[174:177], v[124:127]
	s_waitcnt lgkmcnt(6)
	v_mfma_f32_16x16x32_bf16 v[124:127], v[162:165], v[178:181], v[124:127]
	v_mfma_f32_16x16x32_bf16 v[120:123], v[166:169], v[174:177], v[120:123]
	s_nop 0
	v_mfma_f32_16x16x32_bf16 v[120:123], v[170:173], v[178:181], v[120:123]
	s_waitcnt lgkmcnt(5)
	v_mfma_f32_16x16x32_bf16 v[116:119], v[158:161], v[182:185], v[116:119]
	s_waitcnt lgkmcnt(4)
	v_mfma_f32_16x16x32_bf16 v[116:119], v[162:165], v[186:189], v[116:119]
	v_mfma_f32_16x16x32_bf16 v[112:115], v[166:169], v[182:185], v[112:115]
	s_nop 0
	v_mfma_f32_16x16x32_bf16 v[112:115], v[170:173], v[186:189], v[112:115]
	s_waitcnt lgkmcnt(3)
	v_mfma_f32_16x16x32_bf16 v[108:111], v[158:161], v[190:193], v[108:111]
	s_waitcnt lgkmcnt(2)
	v_mfma_f32_16x16x32_bf16 v[108:111], v[162:165], v[194:197], v[108:111]
	v_mfma_f32_16x16x32_bf16 v[104:107], v[166:169], v[190:193], v[104:107]
	s_nop 0
	v_mfma_f32_16x16x32_bf16 v[104:107], v[170:173], v[194:197], v[104:107]
	s_waitcnt lgkmcnt(1)
	v_mfma_f32_16x16x32_bf16 v[100:103], v[158:161], v[234:237], v[100:103]
	s_waitcnt lgkmcnt(0)
	v_mfma_f32_16x16x32_bf16 v[100:103], v[162:165], v[238:241], v[100:103]
	v_mfma_f32_16x16x32_bf16 v[96:99], v[166:169], v[234:237], v[96:99]
	s_nop 0
	v_mfma_f32_16x16x32_bf16 v[96:99], v[170:173], v[238:241], v[96:99]
	s_setprio 0
	s_setprio 1
	v_mfma_f32_16x16x32_bf16 v[92:95], v[148:151], v[174:177], v[92:95]
	s_nop 0
	v_mfma_f32_16x16x32_bf16 v[92:95], v[144:147], v[178:181], v[92:95]
	v_mfma_f32_16x16x32_bf16 v[88:91], v[140:143], v[174:177], v[88:91]
	s_nop 0
	v_mfma_f32_16x16x32_bf16 v[88:91], v[136:139], v[178:181], v[88:91]
	v_mfma_f32_16x16x32_bf16 v[84:87], v[148:151], v[182:185], v[84:87]
	s_nop 0
	v_mfma_f32_16x16x32_bf16 v[84:87], v[144:147], v[186:189], v[84:87]
	v_mfma_f32_16x16x32_bf16 v[80:83], v[140:143], v[182:185], v[80:83]
	s_nop 0
	v_mfma_f32_16x16x32_bf16 v[80:83], v[136:139], v[186:189], v[80:83]
	v_mfma_f32_16x16x32_bf16 v[76:79], v[148:151], v[190:193], v[76:79]
	s_nop 0
	v_mfma_f32_16x16x32_bf16 v[76:79], v[144:147], v[194:197], v[76:79]
	v_mfma_f32_16x16x32_bf16 v[72:75], v[140:143], v[190:193], v[72:75]
	s_nop 0
	v_mfma_f32_16x16x32_bf16 v[72:75], v[136:139], v[194:197], v[72:75]
	v_mfma_f32_16x16x32_bf16 v[68:71], v[148:151], v[234:237], v[68:71]
	s_nop 0
	v_mfma_f32_16x16x32_bf16 v[68:71], v[144:147], v[238:241], v[68:71]
	v_mfma_f32_16x16x32_bf16 v[64:67], v[140:143], v[234:237], v[64:67]
	s_nop 0
	v_mfma_f32_16x16x32_bf16 v[64:67], v[136:139], v[238:241], v[64:67]
	s_setprio 0
	s_barrier
	ds_read_b128 v[174:177], v232 offset:16384
	ds_read_b128 v[178:181], v232 offset:17408
	ds_read_b128 v[182:185], v232 offset:18432
	ds_read_b128 v[186:189], v232 offset:19456
	ds_read_b128 v[190:193], v232 offset:20480
	ds_read_b128 v[194:197], v232 offset:21504
	ds_read_b128 v[234:237], v232 offset:22528
	ds_read_b128 v[238:241], v232 offset:23552
	s_mov_b32 m0, s47
	s_add_i32 s95, s93, 0x40000
	buffer_load_dwordx4 v214, s[8:11], s93 offen lds
	s_mov_b32 m0, s62
	s_nop 0
	buffer_load_dwordx4 v214, s[8:11], s95 offen lds
	s_add_i32 s95, s93, 0x4000
	s_mov_b32 m0, s63
	s_nop 0
	buffer_load_dwordx4 v214, s[8:11], s95 offen lds
	s_add_i32 s95, s93, 0x44000
	s_mov_b32 m0, s64
	s_nop 0
	buffer_load_dwordx4 v214, s[8:11], s95 offen lds
	s_mov_b32 m0, s46
	s_add_i32 s95, s43, 0x80000
	buffer_load_dwordx4 v213, s[12:15], s43 offen lds
	s_mov_b32 m0, s65
	s_nop 0
	buffer_load_dwordx4 v213, s[12:15], s95 offen lds
	s_waitcnt vmcnt(10)
	s_waitcnt lgkmcnt(0)
	s_barrier
	s_setprio 1
	s_waitcnt lgkmcnt(7)
	v_mfma_f32_16x16x32_bf16 v[60:63], v[158:161], v[174:177], v[60:63]
	s_waitcnt lgkmcnt(6)
	v_mfma_f32_16x16x32_bf16 v[60:63], v[162:165], v[178:181], v[60:63]
	v_mfma_f32_16x16x32_bf16 v[56:59], v[166:169], v[174:177], v[56:59]
	s_nop 0
	v_mfma_f32_16x16x32_bf16 v[56:59], v[170:173], v[178:181], v[56:59]
	s_waitcnt lgkmcnt(5)
	v_mfma_f32_16x16x32_bf16 v[52:55], v[158:161], v[182:185], v[52:55]
	s_waitcnt lgkmcnt(4)
	v_mfma_f32_16x16x32_bf16 v[52:55], v[162:165], v[186:189], v[52:55]
	v_mfma_f32_16x16x32_bf16 v[48:51], v[166:169], v[182:185], v[48:51]
	s_nop 0
	v_mfma_f32_16x16x32_bf16 v[48:51], v[170:173], v[186:189], v[48:51]
	s_waitcnt lgkmcnt(3)
	v_mfma_f32_16x16x32_bf16 v[44:47], v[158:161], v[190:193], v[44:47]
	s_waitcnt lgkmcnt(2)
	v_mfma_f32_16x16x32_bf16 v[44:47], v[162:165], v[194:197], v[44:47]
	v_mfma_f32_16x16x32_bf16 v[40:43], v[166:169], v[190:193], v[40:43]
	s_nop 0
	v_mfma_f32_16x16x32_bf16 v[40:43], v[170:173], v[194:197], v[40:43]
	s_waitcnt lgkmcnt(1)
	v_mfma_f32_16x16x32_bf16 v[36:39], v[158:161], v[234:237], v[36:39]
	s_waitcnt lgkmcnt(0)
	v_mfma_f32_16x16x32_bf16 v[36:39], v[162:165], v[238:241], v[36:39]
	v_mfma_f32_16x16x32_bf16 v[32:35], v[166:169], v[234:237], v[32:35]
	s_nop 0
	v_mfma_f32_16x16x32_bf16 v[32:35], v[170:173], v[238:241], v[32:35]
	s_setprio 0
	s_setprio 1
	v_mfma_f32_16x16x32_bf16 v[28:31], v[148:151], v[174:177], v[28:31]
	s_nop 0
	v_mfma_f32_16x16x32_bf16 v[28:31], v[144:147], v[178:181], v[28:31]
	v_mfma_f32_16x16x32_bf16 v[24:27], v[140:143], v[174:177], v[24:27]
	s_nop 0
	v_mfma_f32_16x16x32_bf16 v[24:27], v[136:139], v[178:181], v[24:27]
	v_mfma_f32_16x16x32_bf16 v[20:23], v[148:151], v[182:185], v[20:23]
	s_nop 0
	v_mfma_f32_16x16x32_bf16 v[20:23], v[144:147], v[186:189], v[20:23]
	v_mfma_f32_16x16x32_bf16 v[16:19], v[140:143], v[182:185], v[16:19]
	s_nop 0
	v_mfma_f32_16x16x32_bf16 v[16:19], v[136:139], v[186:189], v[16:19]
	v_mfma_f32_16x16x32_bf16 v[12:15], v[148:151], v[190:193], v[12:15]
	s_nop 0
	v_mfma_f32_16x16x32_bf16 v[12:15], v[144:147], v[194:197], v[12:15]
	v_mfma_f32_16x16x32_bf16 v[8:11], v[140:143], v[190:193], v[8:11]
	s_nop 0
	v_mfma_f32_16x16x32_bf16 v[8:11], v[136:139], v[194:197], v[8:11]
	v_mfma_f32_16x16x32_bf16 v[4:7], v[148:151], v[234:237], v[4:7]
	s_nop 0
	v_mfma_f32_16x16x32_bf16 v[4:7], v[144:147], v[238:241], v[4:7]
	v_mfma_f32_16x16x32_bf16 v[0:3], v[140:143], v[234:237], v[0:3]
	s_nop 0
	v_mfma_f32_16x16x32_bf16 v[0:3], v[136:139], v[238:241], v[0:3]
	s_setprio 0
	s_barrier
	ds_read_b128 v[136:139], v224
	ds_read_b128 v[140:143], v225
	ds_read_b128 v[144:147], v226
	ds_read_b128 v[148:151], v227
	ds_read_b128 v[158:161], v228
	ds_read_b128 v[162:165], v229
	ds_read_b128 v[166:169], v230
	ds_read_b128 v[170:173], v231
	ds_read_b128 v[174:177], v232 offset:32768
	ds_read_b128 v[178:181], v232 offset:33792
	ds_read_b128 v[182:185], v232 offset:34816
	ds_read_b128 v[186:189], v232 offset:35840
	ds_read_b128 v[190:193], v232 offset:36864
	ds_read_b128 v[194:197], v232 offset:37888
	ds_read_b128 v[234:237], v232 offset:38912
	ds_read_b128 v[238:241], v232 offset:39936
	s_mov_b32 m0, s68
	s_add_i32 s95, s43, 0x100000
	buffer_load_dwordx4 v213, s[12:15], s95 offen lds
	s_add_i32 s95, s43, 0x180000
	s_mov_b32 m0, s69
	s_nop 0
	buffer_load_dwordx4 v213, s[12:15], s95 offen lds
	s_waitcnt vmcnt(10)
	s_waitcnt lgkmcnt(8)
	s_barrier
	s_setprio 1
	s_waitcnt lgkmcnt(7)
	v_mfma_f32_16x16x32_bf16 v[124:127], v[136:139], v[174:177], v[124:127]
	s_waitcnt lgkmcnt(6)
	v_mfma_f32_16x16x32_bf16 v[124:127], v[140:143], v[178:181], v[124:127]
	v_mfma_f32_16x16x32_bf16 v[120:123], v[144:147], v[174:177], v[120:123]
	s_nop 0
	v_mfma_f32_16x16x32_bf16 v[120:123], v[148:151], v[178:181], v[120:123]
	s_waitcnt lgkmcnt(5)
	v_mfma_f32_16x16x32_bf16 v[116:119], v[136:139], v[182:185], v[116:119]
	s_waitcnt lgkmcnt(4)
	v_mfma_f32_16x16x32_bf16 v[116:119], v[140:143], v[186:189], v[116:119]
	v_mfma_f32_16x16x32_bf16 v[112:115], v[144:147], v[182:185], v[112:115]
	s_nop 0
	v_mfma_f32_16x16x32_bf16 v[112:115], v[148:151], v[186:189], v[112:115]
	s_waitcnt lgkmcnt(3)
	v_mfma_f32_16x16x32_bf16 v[108:111], v[136:139], v[190:193], v[108:111]
	s_waitcnt lgkmcnt(2)
	v_mfma_f32_16x16x32_bf16 v[108:111], v[140:143], v[194:197], v[108:111]
	v_mfma_f32_16x16x32_bf16 v[104:107], v[144:147], v[190:193], v[104:107]
	s_nop 0
	v_mfma_f32_16x16x32_bf16 v[104:107], v[148:151], v[194:197], v[104:107]
	s_waitcnt lgkmcnt(1)
	v_mfma_f32_16x16x32_bf16 v[100:103], v[136:139], v[234:237], v[100:103]
	s_waitcnt lgkmcnt(0)
	v_mfma_f32_16x16x32_bf16 v[100:103], v[140:143], v[238:241], v[100:103]
	v_mfma_f32_16x16x32_bf16 v[96:99], v[144:147], v[234:237], v[96:99]
	s_nop 0
	v_mfma_f32_16x16x32_bf16 v[96:99], v[148:151], v[238:241], v[96:99]
	s_setprio 0
	s_setprio 1
	v_mfma_f32_16x16x32_bf16 v[92:95], v[158:161], v[174:177], v[92:95]
	s_nop 0
	v_mfma_f32_16x16x32_bf16 v[92:95], v[162:165], v[178:181], v[92:95]
	v_mfma_f32_16x16x32_bf16 v[88:91], v[166:169], v[174:177], v[88:91]
	s_nop 0
	v_mfma_f32_16x16x32_bf16 v[88:91], v[170:173], v[178:181], v[88:91]
	v_mfma_f32_16x16x32_bf16 v[84:87], v[158:161], v[182:185], v[84:87]
	s_nop 0
	v_mfma_f32_16x16x32_bf16 v[84:87], v[162:165], v[186:189], v[84:87]
	v_mfma_f32_16x16x32_bf16 v[80:83], v[166:169], v[182:185], v[80:83]
	s_nop 0
	v_mfma_f32_16x16x32_bf16 v[80:83], v[170:173], v[186:189], v[80:83]
	v_mfma_f32_16x16x32_bf16 v[76:79], v[158:161], v[190:193], v[76:79]
	s_nop 0
	v_mfma_f32_16x16x32_bf16 v[76:79], v[162:165], v[194:197], v[76:79]
	v_mfma_f32_16x16x32_bf16 v[72:75], v[166:169], v[190:193], v[72:75]
	s_nop 0
	v_mfma_f32_16x16x32_bf16 v[72:75], v[170:173], v[194:197], v[72:75]
	v_mfma_f32_16x16x32_bf16 v[68:71], v[158:161], v[234:237], v[68:71]
	s_nop 0
	v_mfma_f32_16x16x32_bf16 v[68:71], v[162:165], v[238:241], v[68:71]
	v_mfma_f32_16x16x32_bf16 v[64:67], v[166:169], v[234:237], v[64:67]
	s_nop 0
	v_mfma_f32_16x16x32_bf16 v[64:67], v[170:173], v[238:241], v[64:67]
	s_setprio 0
	s_barrier
	ds_read_b128 v[174:177], v232 offset:49152
	ds_read_b128 v[178:181], v232 offset:50176
	ds_read_b128 v[182:185], v232 offset:51200
	ds_read_b128 v[186:189], v232 offset:52224
	ds_read_b128 v[190:193], v232 offset:53248
	ds_read_b128 v[194:197], v232 offset:54272
	ds_read_b128 v[234:237], v232 offset:55296
	ds_read_b128 v[238:241], v232 offset:56320
	s_mov_b32 m0, s72
	s_add_i32 s43, s43, 0x80080
	buffer_load_dwordx4 v214, s[8:11], s94 offen lds
	s_add_i32 s94, s93, 0x40080
	s_mov_b32 m0, s73
	s_nop 0
	buffer_load_dwordx4 v214, s[8:11], s94 offen lds
	s_add_i32 s94, s93, 0x4080
	s_mov_b32 m0, s76
	s_add_i32 s93, s93, 0x44080
	buffer_load_dwordx4 v214, s[8:11], s94 offen lds
	s_mov_b32 m0, s77
	s_nop 0
	buffer_load_dwordx4 v214, s[8:11], s93 offen lds
	s_mov_b32 m0, s74
	s_nop 0
	buffer_load_dwordx4 v213, s[12:15], s92 offen lds
	s_mov_b32 m0, s75
	s_nop 0
	buffer_load_dwordx4 v213, s[12:15], s43 offen lds
	s_waitcnt vmcnt(8)
	s_waitcnt lgkmcnt(0)
	s_barrier
	s_setprio 1
	s_waitcnt lgkmcnt(7)
	v_mfma_f32_16x16x32_bf16 v[60:63], v[136:139], v[174:177], v[60:63]
	s_waitcnt lgkmcnt(6)
	v_mfma_f32_16x16x32_bf16 v[60:63], v[140:143], v[178:181], v[60:63]
	v_mfma_f32_16x16x32_bf16 v[56:59], v[144:147], v[174:177], v[56:59]
	s_nop 0
	v_mfma_f32_16x16x32_bf16 v[56:59], v[148:151], v[178:181], v[56:59]
	s_waitcnt lgkmcnt(5)
	v_mfma_f32_16x16x32_bf16 v[52:55], v[136:139], v[182:185], v[52:55]
	s_waitcnt lgkmcnt(4)
	v_mfma_f32_16x16x32_bf16 v[52:55], v[140:143], v[186:189], v[52:55]
	v_mfma_f32_16x16x32_bf16 v[48:51], v[144:147], v[182:185], v[48:51]
	s_nop 0
	v_mfma_f32_16x16x32_bf16 v[48:51], v[148:151], v[186:189], v[48:51]
	s_waitcnt lgkmcnt(3)
	v_mfma_f32_16x16x32_bf16 v[44:47], v[136:139], v[190:193], v[44:47]
	s_waitcnt lgkmcnt(2)
	v_mfma_f32_16x16x32_bf16 v[44:47], v[140:143], v[194:197], v[44:47]
	v_mfma_f32_16x16x32_bf16 v[40:43], v[144:147], v[190:193], v[40:43]
	s_nop 0
	v_mfma_f32_16x16x32_bf16 v[40:43], v[148:151], v[194:197], v[40:43]
	s_waitcnt lgkmcnt(1)
	v_mfma_f32_16x16x32_bf16 v[36:39], v[136:139], v[234:237], v[36:39]
	s_waitcnt lgkmcnt(0)
	v_mfma_f32_16x16x32_bf16 v[36:39], v[140:143], v[238:241], v[36:39]
	v_mfma_f32_16x16x32_bf16 v[32:35], v[144:147], v[234:237], v[32:35]
	s_nop 0
	v_mfma_f32_16x16x32_bf16 v[32:35], v[148:151], v[238:241], v[32:35]
	s_setprio 0
	s_setprio 1
	v_mfma_f32_16x16x32_bf16 v[28:31], v[158:161], v[174:177], v[28:31]
	s_nop 0
	v_mfma_f32_16x16x32_bf16 v[28:31], v[162:165], v[178:181], v[28:31]
	v_mfma_f32_16x16x32_bf16 v[24:27], v[166:169], v[174:177], v[24:27]
	s_nop 0
	v_mfma_f32_16x16x32_bf16 v[24:27], v[170:173], v[178:181], v[24:27]
	v_mfma_f32_16x16x32_bf16 v[20:23], v[158:161], v[182:185], v[20:23]
	s_nop 0
	v_mfma_f32_16x16x32_bf16 v[20:23], v[162:165], v[186:189], v[20:23]
	v_mfma_f32_16x16x32_bf16 v[16:19], v[166:169], v[182:185], v[16:19]
	s_nop 0
	v_mfma_f32_16x16x32_bf16 v[16:19], v[170:173], v[186:189], v[16:19]
	v_mfma_f32_16x16x32_bf16 v[12:15], v[158:161], v[190:193], v[12:15]
	s_nop 0
	v_mfma_f32_16x16x32_bf16 v[12:15], v[162:165], v[194:197], v[12:15]
	v_mfma_f32_16x16x32_bf16 v[8:11], v[166:169], v[190:193], v[8:11]
	s_nop 0
	v_mfma_f32_16x16x32_bf16 v[8:11], v[170:173], v[194:197], v[8:11]
	v_mfma_f32_16x16x32_bf16 v[4:7], v[158:161], v[234:237], v[4:7]
	s_nop 0
	v_mfma_f32_16x16x32_bf16 v[4:7], v[162:165], v[238:241], v[4:7]
	v_mfma_f32_16x16x32_bf16 v[0:3], v[166:169], v[234:237], v[0:3]
	s_nop 0
	v_mfma_f32_16x16x32_bf16 v[0:3], v[170:173], v[238:241], v[0:3]
	s_setprio 0
	s_barrier
	s_bitcmp0_b32 s42, 0
	s_waitcnt vmcnt(15)
	v_mul_f32_e32 v128, 0x42800000, v128
	s_waitcnt vmcnt(14)
	v_mul_f32_e32 v132, 0x42800000, v132
	v_mul_f32_e32 v129, 0x42800000, v129
	v_mul_f32_e32 v133, 0x42800000, v133
	v_mul_f32_e32 v130, 0x42800000, v130
	v_mul_f32_e32 v134, 0x42800000, v134
	v_mul_f32_e32 v131, 0x42800000, v131
	v_mul_f32_e32 v135, 0x42800000, v135
	s_mov_b64 s[42:43], -1
	s_cbranch_scc0 .LBB0_598
	s_andn2_b64 vcc, exec, s[42:43]
	s_cbranch_vccnz .LBB0_594
	s_branch .LBB0_599
